# passCU loop rewritten (coalesced gathers via LDS staging, Sel from rowptr bitmask, prefetch); hoisted first index/tile loads ahead of prologue barrier in passL/passCU/U2/U3
# speedup vs baseline: 1.0824x; 1.0395x over previous
_Z4k_U2PKtPK15HIP_vector_typeIjLj4EEPKdPKfS8_S8_PtPd:
	s_load_dwordx2 s[4:5], s[0:1], 0x8
	s_load_dwordx2 s[20:21], s[0:1], 0x0
	s_load_dword s22, s[0:1], 0x40
	v_mov_b32_e32 v3, 0
	v_lshlrev_b32_e32 v2, 4, v0
	s_movk_i32 s3, 0x1000
	v_lshlrev_b32_e32 v1, 2, v0
	s_waitcnt lgkmcnt(0)
	v_lshrrev_b32_e32 v60, 6, v0
	v_mul_lo_u32 v60, s22, v60
	v_add_u32_e32 v60, s2, v60
	v_min_u32_e32 v60, 0xc34, v60
	v_and_b32_e32 v61, 31, v0
	v_lshl_or_b32 v60, v60, 5, v61
	v_and_b32_e32 v61, 32, v0
	v_lshlrev_b32_e32 v60, 7, v60
	v_lshl_add_u32 v60, v61, 1, v60
	global_load_dwordx4 v[44:47], v60, s[20:21] offset:48
	global_load_dwordx4 v[48:51], v60, s[20:21] offset:32
	global_load_dwordx4 v[52:55], v60, s[20:21] offset:16
	global_load_dwordx4 v[56:59], v60, s[20:21]
	v_lshl_add_u64 v[16:17], s[4:5], 0, v[2:3]
	v_add_co_u32_e32 v18, vcc, 0x1000, v16
	global_load_dwordx4 v[4:7], v2, s[4:5]
	s_nop 0
	v_addc_co_u32_e32 v19, vcc, 0, v17, vcc
	v_add_co_u32_e32 v20, vcc, 0x2000, v16
	s_nop 1
	v_addc_co_u32_e32 v21, vcc, 0, v17, vcc
	global_load_dwordx4 v[8:11], v[18:19], off
	global_load_dwordx4 v[12:15], v[20:21], off
	v_add_co_u32_e32 v16, vcc, 0x3000, v16
	s_nop 1
	v_addc_co_u32_e32 v17, vcc, 0, v17, vcc
	global_load_dwordx4 v[16:19], v[16:17], off
	v_cmp_gt_u32_e32 vcc, 64, v0
	s_waitcnt vmcnt(3)
	ds_write_b128 v2, v[4:7]
	s_waitcnt vmcnt(2)
	ds_write_b128 v2, v[8:11] offset:4096
	s_waitcnt vmcnt(1)
	ds_write_b128 v2, v[12:15] offset:8192
	s_waitcnt vmcnt(0)
	ds_write_b128 v2, v[16:19] offset:12288
	s_and_saveexec_b64 s[6:7], vcc
	s_cbranch_execz .LBB3_2
	s_load_dwordx4 s[8:11], s[0:1], 0x10
	s_load_dwordx2 s[4:5], s[0:1], 0x20
	v_lshlrev_b32_e32 v4, 3, v0
	v_mov_b32_e32 v5, 0
	s_mov_b32 s12, 0
	s_waitcnt lgkmcnt(0)
	global_load_dwordx2 v[8:9], v4, s[8:9]
	global_load_dwordx2 v[10:11], v4, s[8:9] offset:512
	global_load_dwordx2 v[12:13], v4, s[8:9] offset:1024
	global_load_dwordx2 v[14:15], v4, s[8:9] offset:1536
	global_load_dwordx2 v[16:17], v4, s[8:9] offset:2048
	global_load_dwordx2 v[18:19], v4, s[8:9] offset:2560
	global_load_dwordx2 v[20:21], v4, s[8:9] offset:3072
	global_load_dwordx2 v[22:23], v4, s[8:9] offset:3584
	v_lshl_add_u64 v[6:7], s[8:9], 0, v[4:5]
	v_add_co_u32_e32 v4, vcc, s3, v6
	s_mov_b32 s8, 0x88e368f1
	s_nop 0
	v_addc_co_u32_e32 v5, vcc, 0, v7, vcc
	global_load_dwordx2 v[6:7], v[4:5], off
	global_load_dwordx2 v[24:25], v[4:5], off offset:512
	global_load_dwordx2 v[26:27], v[4:5], off offset:1024
	global_load_dwordx2 v[28:29], v[4:5], off offset:1536
	global_load_dwordx2 v[30:31], v[4:5], off offset:2048
	global_load_dwordx2 v[32:33], v[4:5], off offset:2560
	global_load_dwordx2 v[34:35], v[4:5], off offset:3072
	global_load_dwordx2 v[36:37], v[4:5], off offset:3584
	global_load_dword v2, v1, s[10:11]
	global_load_dword v38, v1, s[4:5]
	s_mov_b32 s10, 0
	s_mov_b32 s11, 0x40f86a00
	s_mov_b32 s9, 0x3ee4f8b5
	s_brev_b32 s13, 8
	v_mov_b32_e32 v39, 0x100
	v_mov_b32_e32 v40, 0xffffff80
	v_mov_b32_e32 v41, 0x260
	s_waitcnt vmcnt(17)
	v_add_f64 v[4:5], v[8:9], 0
	s_waitcnt vmcnt(16)
	v_add_f64 v[8:9], v[10:11], 0
	s_waitcnt vmcnt(15)
	v_add_f64 v[4:5], v[4:5], v[12:13]
	s_waitcnt vmcnt(14)
	v_add_f64 v[8:9], v[8:9], v[14:15]
	s_waitcnt vmcnt(13)
	v_add_f64 v[4:5], v[4:5], v[16:17]
	s_waitcnt vmcnt(12)
	v_add_f64 v[8:9], v[8:9], v[18:19]
	s_waitcnt vmcnt(11)
	v_add_f64 v[4:5], v[4:5], v[20:21]
	s_waitcnt vmcnt(10)
	v_add_f64 v[8:9], v[8:9], v[22:23]
	s_waitcnt vmcnt(9)
	v_add_f64 v[4:5], v[4:5], v[6:7]
	s_waitcnt vmcnt(8)
	v_add_f64 v[6:7], v[8:9], v[24:25]
	s_waitcnt vmcnt(7)
	v_add_f64 v[4:5], v[4:5], v[26:27]
	s_waitcnt vmcnt(6)
	v_add_f64 v[6:7], v[6:7], v[28:29]
	s_waitcnt vmcnt(5)
	v_add_f64 v[4:5], v[4:5], v[30:31]
	s_waitcnt vmcnt(4)
	v_add_f64 v[6:7], v[6:7], v[32:33]
	s_waitcnt vmcnt(3)
	v_add_f64 v[4:5], v[4:5], v[34:35]
	s_waitcnt vmcnt(2)
	v_add_f64 v[6:7], v[6:7], v[36:37]
	v_div_scale_f64 v[8:9], s[4:5], s[10:11], s[10:11], v[4:5]
	v_div_scale_f64 v[12:13], s[4:5], s[10:11], s[10:11], v[6:7]
	v_rcp_f64_e32 v[14:15], v[8:9]
	v_rcp_f64_e32 v[16:17], v[12:13]
	v_div_scale_f64 v[10:11], vcc, v[4:5], s[10:11], v[4:5]
	v_fma_f64 v[20:21], -v[8:9], v[14:15], 1.0
	v_fma_f64 v[22:23], -v[12:13], v[16:17], 1.0
	v_fmac_f64_e32 v[14:15], v[14:15], v[20:21]
	v_fmac_f64_e32 v[16:17], v[16:17], v[22:23]
	v_fma_f64 v[20:21], -v[8:9], v[14:15], 1.0
	v_fma_f64 v[22:23], -v[12:13], v[16:17], 1.0
	v_fmac_f64_e32 v[14:15], v[14:15], v[20:21]
	v_div_scale_f64 v[18:19], s[4:5], v[6:7], s[10:11], v[6:7]
	v_fmac_f64_e32 v[16:17], v[16:17], v[22:23]
	v_mul_f64 v[20:21], v[10:11], v[14:15]
	v_mul_f64 v[22:23], v[18:19], v[16:17]
	v_fma_f64 v[8:9], -v[8:9], v[20:21], v[10:11]
	v_fma_f64 v[10:11], -v[12:13], v[22:23], v[18:19]
	v_div_fmas_f64 v[8:9], v[8:9], v[14:15], v[20:21]
	s_mov_b64 vcc, s[4:5]
	v_div_fixup_f64 v[4:5], v[8:9], s[10:11], v[4:5]
	v_div_fmas_f64 v[8:9], v[10:11], v[16:17], v[22:23]
	v_div_fixup_f64 v[6:7], v[8:9], s[10:11], v[6:7]
	v_fma_f64 v[6:7], -v[4:5], v[4:5], v[6:7]
	v_cmp_ngt_f64_e32 vcc, 0, v[6:7]
	s_waitcnt vmcnt(1)
	v_cvt_f64_f32_e32 v[10:11], v2
	s_waitcnt vmcnt(0)
	v_cvt_f64_f32_e32 v[12:13], v38
	v_cndmask_b32_e32 v7, 0, v7, vcc
	v_cndmask_b32_e32 v6, 0, v6, vcc
	v_add_f64 v[6:7], v[6:7], s[8:9]
	v_cmp_gt_f64_e32 vcc, s[12:13], v[6:7]
	v_add_f64 v[4:5], v[4:5], 0
	s_nop 0
	v_cndmask_b32_e32 v8, 0, v39, vcc
	v_ldexp_f64 v[6:7], v[6:7], v8
	v_rsq_f64_e32 v[8:9], v[6:7]
	v_cndmask_b32_e32 v2, 0, v40, vcc
	v_cmp_class_f64_e32 vcc, v[6:7], v41
	v_mul_f64 v[14:15], v[6:7], v[8:9]
	v_mul_f64 v[8:9], v[8:9], 0.5
	v_fma_f64 v[16:17], -v[8:9], v[14:15], 0.5
	v_fmac_f64_e32 v[14:15], v[14:15], v[16:17]
	v_fmac_f64_e32 v[8:9], v[8:9], v[16:17]
	v_fma_f64 v[16:17], -v[14:15], v[14:15], v[6:7]
	v_fmac_f64_e32 v[14:15], v[16:17], v[8:9]
	v_fma_f64 v[16:17], -v[14:15], v[14:15], v[6:7]
	v_fmac_f64_e32 v[14:15], v[16:17], v[8:9]
	v_ldexp_f64 v[8:9], v[14:15], v2
	v_cndmask_b32_e32 v7, v9, v7, vcc
	v_cndmask_b32_e32 v6, v8, v6, vcc
	v_div_scale_f64 v[8:9], s[4:5], v[6:7], v[6:7], v[10:11]
	v_rcp_f64_e32 v[14:15], v[8:9]
	v_div_scale_f64 v[16:17], vcc, v[10:11], v[6:7], v[10:11]
	v_fma_f64 v[18:19], -v[8:9], v[14:15], 1.0
	v_fmac_f64_e32 v[14:15], v[14:15], v[18:19]
	v_fma_f64 v[18:19], -v[8:9], v[14:15], 1.0
	v_fmac_f64_e32 v[14:15], v[14:15], v[18:19]
	v_mul_f64 v[18:19], v[16:17], v[14:15]
	v_fma_f64 v[8:9], -v[8:9], v[18:19], v[16:17]
	v_div_fmas_f64 v[8:9], v[8:9], v[14:15], v[18:19]
	v_div_fixup_f64 v[6:7], v[8:9], v[6:7], v[10:11]
	v_fma_f64 v[4:5], -v[4:5], v[6:7], v[12:13]
	v_cvt_f32_f64_e32 v2, v[6:7]
	v_cvt_f32_f64_e32 v4, v[4:5]
	ds_write2st64_b32 v1, v2, v4 offset0:72 offset1:73
.LBB3_2:
	s_or_b64 exec, exec, s[6:7]
	s_waitcnt lgkmcnt(0)
	s_barrier
	s_load_dword s3, s[0:1], 0x40
	v_lshrrev_b32_e32 v17, 6, v0
	v_and_b32_e32 v16, 63, v0
	v_mov_b32_e32 v5, 0
	v_mov_b32_e32 v6, 0
	s_waitcnt lgkmcnt(0)
	v_mul_lo_u32 v2, s3, v17
	v_add_u32_e32 v2, s2, v2
	s_movk_i32 s3, 0xc35
	v_cmp_gt_i32_e32 vcc, s3, v2
	v_mov_b32_e32 v7, 0
	s_and_saveexec_b64 s[8:9], vcc
	s_cbranch_execz .LBB3_4
	s_load_dwordx2 s[4:5], s[0:1], 0x0
	v_and_b32_e32 v18, 31, v0
	v_lshlrev_b32_e32 v19, 5, v2
	v_or_b32_e32 v2, v19, v18
	v_ashrrev_i32_e32 v3, 31, v2
	v_lshlrev_b64 v[2:3], 7, v[2:3]
	v_and_b32_e32 v4, 32, v0
	s_waitcnt lgkmcnt(0)
	v_lshl_add_u64 v[2:3], s[4:5], 0, v[2:3]
	v_lshlrev_b32_e32 v14, 1, v4
	v_mov_b32_e32 v15, 0
	v_lshl_add_u64 v[20:21], v[2:3], 0, v[14:15]
	s_waitcnt vmcnt(0)
	v_mov_b32_e32 v2, v44
	v_mov_b32_e32 v3, v45
	v_mov_b32_e32 v4, v46
	v_mov_b32_e32 v5, v47
	v_mov_b32_e32 v6, v48
	v_mov_b32_e32 v7, v49
	v_mov_b32_e32 v8, v50
	v_mov_b32_e32 v9, v51
	v_mov_b32_e32 v10, v52
	v_mov_b32_e32 v11, v53
	v_mov_b32_e32 v12, v54
	v_mov_b32_e32 v13, v55
	v_mov_b32_e32 v22, v56
	v_mov_b32_e32 v23, v57
	v_mov_b32_e32 v24, v58
	v_mov_b32_e32 v25, v59
	s_load_dwordx4 s[4:7], s[0:1], 0x28
	v_lshlrev_b32_e32 v14, 3, v18
	v_and_b32_e32 v20, 0x80, v1
	s_waitcnt vmcnt(0)
	s_waitcnt lgkmcnt(0)
	global_load_dwordx2 a[0:1], v14, s[4:5]
	v_lshlrev_b32_e32 v21, 16, v22
	v_and_b32_e32 v50, 0xffff0000, v22
	v_lshlrev_b32_e32 v51, 16, v23
	v_and_b32_e32 v46, 0xffff0000, v23
	v_lshlrev_b32_e32 v54, 16, v24
	v_and_b32_e32 v55, 0xffff0000, v24
	v_lshlrev_b32_e32 v56, 16, v25
	v_and_b32_e32 v52, 0xffff0000, v25
	v_lshlrev_b32_e32 v57, 16, v10
	v_and_b32_e32 v58, 0xffff0000, v10
	v_lshlrev_b32_e32 v59, 16, v11
	v_and_b32_e32 v60, 0xffff0000, v11
	v_lshlrev_b32_e32 v61, 16, v12
	v_and_b32_e32 v62, 0xffff0000, v12
	v_lshlrev_b32_e32 v63, 16, v13
	v_and_b32_e32 v64, 0xffff0000, v13
	ds_read_b128 v[10:13], v20 offset:18432
	ds_read_b128 v[22:25], v20 offset:18688
	ds_read_b128 v[26:29], v20 offset:18448
	ds_read_b128 v[30:33], v20 offset:18704
	ds_read_b128 v[34:37], v20 offset:18464
	ds_read_b128 v[38:41], v20 offset:18480
	ds_read_b128 v[42:45], v20 offset:18720
	v_lshlrev_b32_e32 v14, 4, v16
	s_waitcnt lgkmcnt(3)
	v_fmac_f32_e32 v33, v29, v52
	v_lshlrev_b32_e32 v65, 16, v6
	v_fmac_f32_e32 v25, v13, v46
	v_fma_f32 v21, v10, v21, v22
	v_fma_f32 v22, v11, v50, v23
	v_fma_f32 v23, v12, v51, v24
	v_fma_f32 v24, v26, v54, v30
	v_fma_f32 v54, v27, v55, v31
	v_fma_f32 v55, v28, v56, v32
	v_max_f32_e32 v25, 0, v25
	v_max_f32_e32 v21, 0, v21
	v_max_f32_e32 v22, 0, v22
	v_max_f32_e32 v23, 0, v23
	s_waitcnt lgkmcnt(0)
	v_fma_f32 v42, v34, v57, v42
	v_max_f32_e32 v34, 0, v33
	v_cvt_pk_f16_f32 v22, v21, v22
	v_cvt_pk_f16_f32 v23, v23, v25
	v_max_f32_e32 v21, 0, v24
	v_max_f32_e32 v24, 0, v54
	v_max_f32_e32 v25, 0, v55
	ds_read_b128 v[50:53], v14
	ds_read_b128 v[10:13], v14 offset:1024
	v_cvt_pk_f16_f32 v24, v21, v24
	v_cvt_pk_f16_f32 v25, v25, v34
	ds_read_b128 v[26:29], v14 offset:4096
	v_and_b32_e32 v66, 0xffff0000, v6
	v_lshlrev_b32_e32 v67, 16, v7
	v_and_b32_e32 v68, 0xffff0000, v7
	v_lshlrev_b32_e32 v69, 16, v8
	v_and_b32_e32 v70, 0xffff0000, v8
	v_lshlrev_b32_e32 v56, 16, v9
	v_and_b32_e32 v57, 0xffff0000, v9
	ds_read_b128 v[6:9], v14 offset:5120
	ds_read_b128 v[30:33], v14 offset:8192
	ds_read_b128 v[46:49], v20 offset:18736
	v_fmac_f32_e32 v45, v37, v60
	v_fma_f32 v43, v35, v58, v43
	v_fma_f32 v44, v36, v59, v44
	ds_read_b128 v[34:37], v14 offset:9216
	v_lshlrev_b32_e32 v21, 16, v2
	s_waitcnt lgkmcnt(1)
	v_fmac_f32_e32 v49, v41, v64
	v_and_b32_e32 v54, 0xffff0000, v2
	v_fma_f32 v2, v38, v61, v46
	v_fma_f32 v38, v39, v62, v47
	v_fma_f32 v39, v40, v63, v48
	v_lshlrev_b32_e32 v55, 16, v3
	v_and_b32_e32 v58, 0xffff0000, v3
	v_max_f32_e32 v3, 0, v45
	v_max_f32_e32 v40, 0, v42
	v_max_f32_e32 v2, 0, v2
	v_lshlrev_b32_e32 v59, 16, v4
	s_waitcnt vmcnt(0)
	v_accvgpr_mov_b32 a16, a0
	v_accvgpr_mov_b32 a17, a0
	v_accvgpr_mov_b32 a18, a0
	v_accvgpr_mov_b32 a19, a0
	v_accvgpr_mov_b32 a20, a0
	v_accvgpr_mov_b32 a21, a0
	v_accvgpr_mov_b32 a22, a0
	v_accvgpr_mov_b32 a23, a0
	v_accvgpr_mov_b32 a24, a0
	v_accvgpr_mov_b32 a25, a0
	v_accvgpr_mov_b32 a26, a0
	v_accvgpr_mov_b32 a27, a0
	v_accvgpr_mov_b32 a28, a0
	v_accvgpr_mov_b32 a29, a0
	v_accvgpr_mov_b32 a30, a0
	v_accvgpr_mov_b32 a31, a0
	v_accvgpr_mov_b32 a0, a1
	v_accvgpr_mov_b32 a2, a1
	v_mfma_f32_32x32x16_f16 a[16:31], v[22:25], v[50:53], a[16:31]
	v_accvgpr_mov_b32 a3, a1
	v_accvgpr_mov_b32 a4, a1
	v_accvgpr_mov_b32 a5, a1
	v_accvgpr_mov_b32 a6, a1
	v_accvgpr_mov_b32 a7, a1
	v_accvgpr_mov_b32 a8, a1
	v_accvgpr_mov_b32 a9, a1
	v_accvgpr_mov_b32 a10, a1
	v_accvgpr_mov_b32 a11, a1
	v_accvgpr_mov_b32 a12, a1
	v_accvgpr_mov_b32 a13, a1
	v_accvgpr_mov_b32 a14, a1
	v_accvgpr_mov_b32 a15, a1
	ds_read_b128 v[50:53], v14 offset:12288
	v_mfma_f32_32x32x16_f16 a[16:31], v[22:25], v[30:33], a[16:31]
	v_max_f32_e32 v30, 0, v43
	v_max_f32_e32 v31, 0, v44
	v_max_f32_e32 v32, 0, v38
	v_max_f32_e32 v33, 0, v39
	v_max_f32_e32 v38, 0, v49
	v_cvt_pk_f16_f32 v30, v40, v30
	v_cvt_pk_f16_f32 v31, v31, v3
	v_mfma_f32_32x32x16_f16 a[0:15], v[22:25], v[26:29], a[0:15]
	ds_read_b128 v[26:29], v14 offset:13312
	v_cvt_pk_f16_f32 v32, v2, v32
	v_cvt_pk_f16_f32 v33, v33, v38
	s_waitcnt lgkmcnt(1)
	v_mfma_f32_32x32x16_f16 a[0:15], v[22:25], v[50:53], a[0:15]
	ds_read_b128 v[22:25], v20 offset:18752
	ds_read_b128 v[38:41], v20 offset:18496
	ds_read_b128 v[42:45], v20 offset:18512
	ds_read_b128 v[46:49], v20 offset:18768
	v_and_b32_e32 v50, 0xffff0000, v4
	v_lshlrev_b32_e32 v51, 16, v5
	v_and_b32_e32 v52, 0xffff0000, v5
	s_waitcnt lgkmcnt(2)
	v_fma_f32 v2, v38, v65, v22
	v_fma_f32 v3, v39, v66, v23
	v_fma_f32 v4, v40, v67, v24
	v_mfma_f32_32x32x16_f16 a[16:31], v[30:33], v[10:13], a[16:31]
	v_fmac_f32_e32 v25, v41, v68
	s_waitcnt lgkmcnt(0)
	v_fma_f32 v5, v42, v69, v46
	v_fmac_f32_e32 v49, v45, v57
	v_max_f32_e32 v2, 0, v2
	v_max_f32_e32 v3, 0, v3
	v_max_f32_e32 v4, 0, v4
	v_max_f32_e32 v5, 0, v5
	v_mfma_f32_32x32x16_f16 a[0:15], v[30:33], v[6:9], a[0:15]
	v_fma_f32 v6, v43, v70, v47
	v_fma_f32 v7, v44, v56, v48
	v_max_f32_e32 v8, 0, v25
	v_max_f32_e32 v6, 0, v6
	v_max_f32_e32 v7, 0, v7
	v_max_f32_e32 v9, 0, v49
	ds_read_b128 v[10:13], v14 offset:2048
	v_mfma_f32_32x32x16_f16 a[16:31], v[30:33], v[34:37], a[16:31]
	v_cvt_pk_f16_f32 v2, v2, v3
	v_cvt_pk_f16_f32 v3, v4, v8
	v_cvt_pk_f16_f32 v4, v5, v6
	v_cvt_pk_f16_f32 v5, v7, v9
	v_mfma_f32_32x32x16_f16 a[0:15], v[30:33], v[26:29], a[0:15]
	ds_read_b128 v[6:9], v14 offset:3072
	ds_read_b128 v[22:25], v20 offset:18528
	ds_read_b128 v[26:29], v20 offset:18544
	ds_read_b128 v[30:33], v20 offset:18784
	s_waitcnt lgkmcnt(0)
	v_fmac_f32_e32 v33, v25, v58
	v_mfma_f32_32x32x16_f16 a[16:31], v[2:5], v[10:13], a[16:31]
	ds_read_b128 v[10:13], v14 offset:6144
	ds_read_b128 v[34:37], v20 offset:18800
	ds_read_b128 v[38:41], v14 offset:10240
	ds_read_b128 v[42:45], v14 offset:14336
	v_fma_f32 v20, v22, v21, v30
	v_fma_f32 v21, v23, v54, v31
	v_fma_f32 v22, v24, v55, v32
	s_waitcnt lgkmcnt(2)
	v_fmac_f32_e32 v37, v29, v52
	v_mfma_f32_32x32x16_f16 a[0:15], v[2:5], v[10:13], a[0:15]
	v_fma_f32 v10, v26, v59, v34
	v_fma_f32 v11, v27, v50, v35
	v_fma_f32 v12, v28, v51, v36
	v_max_f32_e32 v13, 0, v20
	v_max_f32_e32 v20, 0, v21
	v_max_f32_e32 v21, 0, v22
	v_max_f32_e32 v22, 0, v33
	s_waitcnt lgkmcnt(1)
	v_mfma_f32_32x32x16_f16 a[16:31], v[2:5], v[38:41], a[16:31]
	v_max_f32_e32 v23, 0, v10
	v_max_f32_e32 v24, 0, v11
	v_max_f32_e32 v25, 0, v12
	v_max_f32_e32 v26, 0, v37
	v_cvt_pk_f16_f32 v10, v13, v20
	v_cvt_pk_f16_f32 v11, v21, v22
	v_cvt_pk_f16_f32 v12, v23, v24
	s_waitcnt lgkmcnt(0)
	v_mfma_f32_32x32x16_f16 a[0:15], v[2:5], v[42:45], a[0:15]
	v_cvt_pk_f16_f32 v13, v25, v26
	ds_read_b128 v[2:5], v14 offset:7168
	s_nop 0
	v_mfma_f32_32x32x16_f16 a[16:31], v[10:13], v[6:9], a[16:31]
	s_waitcnt lgkmcnt(0)
	v_mfma_f32_32x32x16_f16 a[0:15], v[10:13], v[2:5], a[0:15]
	ds_read_b128 v[2:5], v14 offset:11264
	s_waitcnt lgkmcnt(0)
	v_mfma_f32_32x32x16_f16 a[16:31], v[10:13], v[2:5], a[16:31]
	ds_read_b128 v[2:5], v14 offset:15360
	v_lshrrev_b32_e32 v14, 3, v0
	v_and_or_b32 v40, v14, 4, v19
	v_lshlrev_b32_e32 v14, 2, v18
	v_ashrrev_i32_e32 v41, 31, v40
	v_lshl_add_u64 v[14:15], s[6:7], 0, v[14:15]
	s_waitcnt lgkmcnt(0)
	v_mfma_f32_32x32x16_f16 a[0:15], v[10:13], v[2:5], a[0:15]
	s_nop 3
	v_accvgpr_read_b32 v19, a16
	v_accvgpr_read_b32 v38, a16
	v_accvgpr_read_b32 v36, a17
	v_accvgpr_read_b32 v34, a18
	v_accvgpr_read_b32 v32, a19
	v_accvgpr_read_b32 v30, a20
	v_accvgpr_read_b32 v28, a21
	v_accvgpr_read_b32 v26, a22
	v_accvgpr_read_b32 v18, a0
	v_cvt_pk_bf16_f32 v42, v19, v18
	v_lshlrev_b64 v[18:19], 7, v[40:41]
	v_lshl_add_u64 v[18:19], v[14:15], 0, v[18:19]
	global_store_dword v[18:19], v42, off
	v_accvgpr_read_b32 v18, a1
	v_accvgpr_read_b32 v19, a17
	v_cvt_pk_bf16_f32 v41, v19, v18
	v_or_b32_e32 v18, 1, v40
	v_ashrrev_i32_e32 v19, 31, v18
	v_lshlrev_b64 v[18:19], 7, v[18:19]
	v_lshl_add_u64 v[18:19], v[14:15], 0, v[18:19]
	global_store_dword v[18:19], v41, off
	v_accvgpr_read_b32 v18, a2
	v_accvgpr_read_b32 v19, a18
	v_cvt_pk_bf16_f32 v41, v19, v18
	v_or_b32_e32 v18, 2, v40
	v_ashrrev_i32_e32 v19, 31, v18
	v_lshlrev_b64 v[18:19], 7, v[18:19]
	v_lshl_add_u64 v[18:19], v[14:15], 0, v[18:19]
	global_store_dword v[18:19], v41, off
	v_accvgpr_read_b32 v18, a3
	v_accvgpr_read_b32 v19, a19
	v_cvt_pk_bf16_f32 v41, v19, v18
	v_or_b32_e32 v18, 3, v40
	v_ashrrev_i32_e32 v19, 31, v18
	v_lshlrev_b64 v[18:19], 7, v[18:19]
	v_lshl_add_u64 v[18:19], v[14:15], 0, v[18:19]
	global_store_dword v[18:19], v41, off
	v_accvgpr_read_b32 v18, a4
	v_accvgpr_read_b32 v19, a20
	v_cvt_pk_bf16_f32 v41, v19, v18
	v_or_b32_e32 v18, 8, v40
	v_ashrrev_i32_e32 v19, 31, v18
	v_lshlrev_b64 v[18:19], 7, v[18:19]
	v_lshl_add_u64 v[18:19], v[14:15], 0, v[18:19]
	global_store_dword v[18:19], v41, off
	v_accvgpr_read_b32 v18, a5
	v_accvgpr_read_b32 v19, a21
	v_cvt_pk_bf16_f32 v41, v19, v18
	v_or_b32_e32 v18, 9, v40
	v_ashrrev_i32_e32 v19, 31, v18
	v_lshlrev_b64 v[18:19], 7, v[18:19]
	v_lshl_add_u64 v[18:19], v[14:15], 0, v[18:19]
	global_store_dword v[18:19], v41, off
	v_accvgpr_read_b32 v18, a6
	v_accvgpr_read_b32 v19, a22
	v_cvt_pk_bf16_f32 v41, v19, v18
	v_or_b32_e32 v18, 10, v40
	v_ashrrev_i32_e32 v19, 31, v18
	v_lshlrev_b64 v[18:19], 7, v[18:19]
	v_lshl_add_u64 v[18:19], v[14:15], 0, v[18:19]
	global_store_dword v[18:19], v41, off
	v_accvgpr_read_b32 v18, a7
	v_accvgpr_read_b32 v19, a23
	v_cvt_pk_bf16_f32 v41, v19, v18
	v_or_b32_e32 v18, 11, v40
	v_ashrrev_i32_e32 v19, 31, v18
	v_lshlrev_b64 v[18:19], 7, v[18:19]
	v_lshl_add_u64 v[18:19], v[14:15], 0, v[18:19]
	global_store_dword v[18:19], v41, off
	v_accvgpr_read_b32 v18, a8
	v_accvgpr_read_b32 v19, a24
	v_cvt_pk_bf16_f32 v41, v19, v18
	v_or_b32_e32 v18, 16, v40
	v_ashrrev_i32_e32 v19, 31, v18
	v_lshlrev_b64 v[18:19], 7, v[18:19]
	v_lshl_add_u64 v[18:19], v[14:15], 0, v[18:19]
	global_store_dword v[18:19], v41, off
	v_accvgpr_read_b32 v18, a9
	v_accvgpr_read_b32 v19, a25
	v_cvt_pk_bf16_f32 v41, v19, v18
	v_or_b32_e32 v18, 17, v40
	v_ashrrev_i32_e32 v19, 31, v18
	v_lshlrev_b64 v[18:19], 7, v[18:19]
	v_lshl_add_u64 v[18:19], v[14:15], 0, v[18:19]
	global_store_dword v[18:19], v41, off
	v_accvgpr_read_b32 v18, a10
	v_accvgpr_read_b32 v19, a26
	v_cvt_pk_bf16_f32 v41, v19, v18
	v_or_b32_e32 v18, 18, v40
	v_ashrrev_i32_e32 v19, 31, v18
	v_lshlrev_b64 v[18:19], 7, v[18:19]
	v_lshl_add_u64 v[18:19], v[14:15], 0, v[18:19]
	global_store_dword v[18:19], v41, off
	v_accvgpr_read_b32 v18, a11
	v_accvgpr_read_b32 v19, a27
	v_cvt_pk_bf16_f32 v41, v19, v18
	v_or_b32_e32 v18, 19, v40
	v_ashrrev_i32_e32 v19, 31, v18
	v_lshlrev_b64 v[18:19], 7, v[18:19]
	v_lshl_add_u64 v[18:19], v[14:15], 0, v[18:19]
	global_store_dword v[18:19], v41, off
	v_accvgpr_read_b32 v18, a12
	v_accvgpr_read_b32 v19, a28
	v_cvt_pk_bf16_f32 v41, v19, v18
	v_or_b32_e32 v18, 24, v40
	v_ashrrev_i32_e32 v19, 31, v18
	v_lshlrev_b64 v[18:19], 7, v[18:19]
	v_lshl_add_u64 v[18:19], v[14:15], 0, v[18:19]
	global_store_dword v[18:19], v41, off
	v_accvgpr_read_b32 v18, a13
	v_accvgpr_read_b32 v19, a29
	v_cvt_pk_bf16_f32 v41, v19, v18
	v_or_b32_e32 v18, 25, v40
	v_ashrrev_i32_e32 v19, 31, v18
	v_lshlrev_b64 v[18:19], 7, v[18:19]
	v_lshl_add_u64 v[18:19], v[14:15], 0, v[18:19]
	global_store_dword v[18:19], v41, off
	v_accvgpr_read_b32 v18, a14
	v_accvgpr_read_b32 v19, a30
	v_cvt_pk_bf16_f32 v41, v19, v18
	v_or_b32_e32 v18, 26, v40
	v_ashrrev_i32_e32 v19, 31, v18
	v_lshlrev_b64 v[18:19], 7, v[18:19]
	v_lshl_add_u64 v[18:19], v[14:15], 0, v[18:19]
	global_store_dword v[18:19], v41, off
	v_accvgpr_read_b32 v18, a15
	v_accvgpr_read_b32 v19, a31
	v_cvt_pk_bf16_f32 v41, v19, v18
	v_or_b32_e32 v18, 27, v40
	v_ashrrev_i32_e32 v19, 31, v18
	v_lshlrev_b64 v[18:19], 7, v[18:19]
	v_accvgpr_read_b32 v39, a0
	v_lshl_add_u64 v[14:15], v[14:15], 0, v[18:19]
	v_accvgpr_read_b32 v37, a1
	global_store_dword v[14:15], v41, off
	v_pk_add_f32 v[14:15], v[38:39], 0 op_sel_hi:[1,0]
	v_accvgpr_read_b32 v35, a2
	v_pk_add_f32 v[14:15], v[14:15], v[36:37]
	v_pk_fma_f32 v[18:19], v[38:39], v[38:39], 0 op_sel_hi:[1,1,0]
	v_accvgpr_read_b32 v33, a3
	v_pk_add_f32 v[14:15], v[14:15], v[34:35]
	v_pk_fma_f32 v[18:19], v[36:37], v[36:37], v[18:19]
	v_accvgpr_read_b32 v31, a4
	v_pk_add_f32 v[14:15], v[14:15], v[32:33]
	v_pk_fma_f32 v[18:19], v[34:35], v[34:35], v[18:19]
	v_accvgpr_read_b32 v29, a5
	v_pk_add_f32 v[14:15], v[14:15], v[30:31]
	v_pk_fma_f32 v[18:19], v[32:33], v[32:33], v[18:19]
	v_accvgpr_read_b32 v27, a6
	v_pk_add_f32 v[14:15], v[14:15], v[28:29]
	v_pk_fma_f32 v[18:19], v[30:31], v[30:31], v[18:19]
	v_accvgpr_read_b32 v24, a23
	v_accvgpr_read_b32 v25, a7
	v_pk_add_f32 v[14:15], v[14:15], v[26:27]
	v_pk_fma_f32 v[18:19], v[28:29], v[28:29], v[18:19]
	v_accvgpr_read_b32 v22, a24
	v_accvgpr_read_b32 v23, a8
	v_pk_fma_f32 v[18:19], v[26:27], v[26:27], v[18:19]
	v_pk_add_f32 v[14:15], v[14:15], v[24:25]
	v_accvgpr_read_b32 v20, a25
	v_accvgpr_read_b32 v21, a9
	v_pk_add_f32 v[14:15], v[14:15], v[22:23]
	v_pk_fma_f32 v[18:19], v[24:25], v[24:25], v[18:19]
	v_accvgpr_read_b32 v12, a26
	v_accvgpr_read_b32 v13, a10
	v_pk_add_f32 v[14:15], v[14:15], v[20:21]
	v_pk_fma_f32 v[18:19], v[22:23], v[22:23], v[18:19]
	v_accvgpr_read_b32 v10, a27
	v_accvgpr_read_b32 v11, a11
	v_pk_add_f32 v[14:15], v[14:15], v[12:13]
	v_pk_fma_f32 v[18:19], v[20:21], v[20:21], v[18:19]
	v_accvgpr_read_b32 v8, a28
	v_accvgpr_read_b32 v9, a12
	v_pk_add_f32 v[14:15], v[14:15], v[10:11]
	v_pk_fma_f32 v[12:13], v[12:13], v[12:13], v[18:19]
	v_accvgpr_read_b32 v6, a29
	v_accvgpr_read_b32 v7, a13
	v_pk_add_f32 v[14:15], v[14:15], v[8:9]
	v_pk_fma_f32 v[10:11], v[10:11], v[10:11], v[12:13]
	v_accvgpr_read_b32 v4, a30
	v_accvgpr_read_b32 v5, a14
	v_pk_add_f32 v[14:15], v[14:15], v[6:7]
	v_pk_fma_f32 v[8:9], v[8:9], v[8:9], v[10:11]
	v_accvgpr_read_b32 v2, a31
	v_accvgpr_read_b32 v3, a15
	v_pk_add_f32 v[14:15], v[14:15], v[4:5]
	v_pk_fma_f32 v[6:7], v[6:7], v[6:7], v[8:9]
	s_nop 0
	v_pk_fma_f32 v[6:7], v[4:5], v[4:5], v[6:7]
	v_pk_add_f32 v[4:5], v[14:15], v[2:3]
	v_pk_fma_f32 v[6:7], v[2:3], v[2:3], v[6:7]
	v_mov_b32_e32 v3, v4

	.amdhsa_kernel _Z4k_U2PKtPK15HIP_vector_typeIjLj4EEPKdPKfS8_S8_PtPd
		.amdhsa_group_segment_fixed_size 18944
		.amdhsa_private_segment_fixed_size 0
		.amdhsa_kernarg_size 320
		.amdhsa_user_sgpr_count 2
		.amdhsa_user_sgpr_dispatch_ptr 0
		.amdhsa_user_sgpr_queue_ptr 0
		.amdhsa_user_sgpr_kernarg_segment_ptr 1
		.amdhsa_user_sgpr_dispatch_id 0
		.amdhsa_user_sgpr_kernarg_preload_length 0
		.amdhsa_user_sgpr_kernarg_preload_offset 0
		.amdhsa_user_sgpr_private_segment_size 0
		.amdhsa_uses_dynamic_stack 0
		.amdhsa_enable_private_segment 0
		.amdhsa_system_sgpr_workgroup_id_x 1
		.amdhsa_system_sgpr_workgroup_id_y 0
		.amdhsa_system_sgpr_workgroup_id_z 0
		.amdhsa_system_sgpr_workgroup_info 0
		.amdhsa_system_vgpr_workitem_id 0
		.amdhsa_next_free_vgpr 104
		.amdhsa_next_free_sgpr 24
		.amdhsa_accum_offset 72
		.amdhsa_reserve_vcc 1
		.amdhsa_float_round_mode_32 0
		.amdhsa_float_round_mode_16_64 0
		.amdhsa_float_denorm_mode_32 3
		.amdhsa_float_denorm_mode_16_64 3
		.amdhsa_dx10_clamp 1
		.amdhsa_ieee_mode 1
		.amdhsa_fp16_overflow 0
		.amdhsa_tg_split 0
		.amdhsa_exception_fp_ieee_invalid_op 0
		.amdhsa_exception_fp_denorm_src 0
		.amdhsa_exception_fp_ieee_div_zero 0
		.amdhsa_exception_fp_ieee_overflow 0
		.amdhsa_exception_fp_ieee_underflow 0
		.amdhsa_exception_fp_ieee_inexact 0
		.amdhsa_exception_int_div_zero 0
	.end_amdhsa_kernel

_Z7k_passLILi1ELi0ELi1EEvPKiS1_PKfPKtS5_S3_S3_S3_S3_S3_S3_PK15HIP_vector_typeIjLj4EEPKdPdS1_PtS1_:
	s_load_dwordx2 s[4:5], s[0:1], 0x58
	s_load_dwordx4 s[40:43], s[0:1], 0x0
	s_load_dwordx4 s[44:47], s[0:1], 0x10
	s_load_dwordx2 s[48:49], s[0:1], 0x20
	v_mov_b32_e32 v19, 0
	v_lshlrev_b32_e32 v18, 4, v0
	s_mov_b32 s8, 0
	v_readfirstlane_b32 s3, v0
	s_waitcnt lgkmcnt(0)
	s_lshr_b32 s50, s3, 6
	s_lshl_b32 s51, s2, 2
	s_add_i32 s50, s50, s51
	s_mul_i32 s50, s50, 0x7a12
	s_lshr_b32 s50, s50, 12
	s_lshl_b32 s50, s50, 7
	v_lshrrev_b32_e32 v116, 3, v0
	v_and_b32_e32 v116, 7, v116
	v_lshlrev_b32_e32 v116, 4, v116
	v_add_u32_e32 v117, s50, v116
	global_load_dwordx4 v[92:95], v117, s[40:41]
	global_load_dwordx4 v[96:99], v117, s[42:43]
	global_load_dwordx4 v[100:103], v117, s[44:45]
	v_lshl_add_u64 v[2:3], s[4:5], 0, v[18:19]
	v_add_co_u32_e32 v10, vcc, 0x1000, v2
	s_nop 1
	v_addc_co_u32_e32 v11, vcc, 0, v3, vcc
	global_load_dwordx4 v[2:5], v18, s[4:5]
	global_load_dwordx4 v[6:9], v[10:11], off
	s_movk_i32 s4, 0x1000
	v_cmp_gt_u32_e32 vcc, 64, v0
	s_waitcnt vmcnt(1)
	ds_write_b128 v18, v[2:5]
	s_waitcnt vmcnt(0)
	ds_write_b128 v18, v[6:9] offset:4096
	v_and_b32_e32 v118, 7, v0
	v_lshlrev_b32_e32 v118, 4, v118
	v_lshl_or_b32 v42, v96, 7, v118
	v_lshl_or_b32 v46, v92, 7, v118
	v_lshl_or_b32 v43, v97, 7, v118
	v_lshl_or_b32 v47, v93, 7, v118
	v_lshl_or_b32 v44, v98, 7, v118
	v_lshl_or_b32 v48, v94, 7, v118
	v_lshl_or_b32 v45, v99, 7, v118
	v_lshl_or_b32 v49, v95, 7, v118
	global_load_dwordx4 v[60:63], v42, s[46:47]
	global_load_dwordx4 v[76:79], v46, s[48:49]
	global_load_dwordx4 v[64:67], v43, s[46:47]
	global_load_dwordx4 v[80:83], v47, s[48:49]
	global_load_dwordx4 v[68:71], v44, s[46:47]
	global_load_dwordx4 v[84:87], v48, s[48:49]
	global_load_dwordx4 v[72:75], v45, s[46:47]
	global_load_dwordx4 v[88:91], v49, s[48:49]
	s_add_i32 s51, s50, 0x80
	s_min_u32 s51, s51, 0x3d0880
	v_add_u32_e32 v117, s51, v116
	global_load_dwordx4 v[104:107], v117, s[40:41]
	global_load_dwordx4 v[108:111], v117, s[42:43]
	global_load_dwordx4 v[112:115], v117, s[44:45]
	s_and_saveexec_b64 s[10:11], vcc
	s_cbranch_execz .LBB7_2
	s_load_dwordx2 s[6:7], s[0:1], 0x60
	v_lshlrev_b32_e32 v18, 3, v0
	v_lshlrev_b32_e32 v1, 2, v0
	s_mov_b32 s14, 0
	s_brev_b32 s15, 8
	s_waitcnt lgkmcnt(0)
	global_load_dwordx2 v[2:3], v18, s[6:7]
	global_load_dwordx2 v[4:5], v18, s[6:7] offset:512
	global_load_dwordx2 v[6:7], v18, s[6:7] offset:1024
	global_load_dwordx2 v[8:9], v18, s[6:7] offset:1536
	global_load_dwordx2 v[10:11], v18, s[6:7] offset:2048
	global_load_dwordx2 v[12:13], v18, s[6:7] offset:2560
	global_load_dwordx2 v[14:15], v18, s[6:7] offset:3072
	global_load_dwordx2 v[16:17], v18, s[6:7] offset:3584
	v_lshl_add_u64 v[20:21], s[6:7], 0, v[18:19]
	v_add_co_u32_e32 v20, vcc, s4, v20
	v_mov_b32_e32 v39, 0x100
	s_nop 0
	v_addc_co_u32_e32 v21, vcc, 0, v21, vcc
	global_load_dwordx2 v[18:19], v[20:21], off
	global_load_dwordx2 v[22:23], v[20:21], off offset:512
	global_load_dwordx2 v[24:25], v[20:21], off offset:1024
	global_load_dwordx2 v[26:27], v[20:21], off offset:1536
	global_load_dwordx2 v[28:29], v[20:21], off offset:2048
	global_load_dwordx2 v[30:31], v[20:21], off offset:2560
	global_load_dwordx2 v[32:33], v[20:21], off offset:3072
	global_load_dwordx2 v[34:35], v[20:21], off offset:3584
	s_load_dwordx4 s[4:7], s[0:1], 0x28
	s_load_dwordx2 s[12:13], s[0:1], 0x38
	s_waitcnt lgkmcnt(0)
	global_load_dword v36, v1, s[6:7]
	global_load_dword v37, v1, s[4:5]
	global_load_dword v38, v1, s[12:13]
	s_mov_b32 s6, 0
	s_mov_b32 s7, 0x412e8480
	s_mov_b32 s12, 0x88e368f1
	s_mov_b32 s13, 0x3ee4f8b5
	v_mov_b32_e32 v40, 0xffffff80
	v_mov_b32_e32 v41, 0x260
	s_waitcnt vmcnt(18)
	v_add_f64 v[2:3], v[2:3], 0
	s_waitcnt vmcnt(17)
	v_add_f64 v[4:5], v[4:5], 0
	s_waitcnt vmcnt(16)
	v_add_f64 v[2:3], v[2:3], v[6:7]
	s_waitcnt vmcnt(15)
	v_add_f64 v[4:5], v[4:5], v[8:9]
	s_waitcnt vmcnt(14)
	v_add_f64 v[2:3], v[2:3], v[10:11]
	s_waitcnt vmcnt(13)
	v_add_f64 v[4:5], v[4:5], v[12:13]
	s_waitcnt vmcnt(12)
	v_add_f64 v[2:3], v[2:3], v[14:15]
	s_waitcnt vmcnt(11)
	v_add_f64 v[4:5], v[4:5], v[16:17]
	s_waitcnt vmcnt(10)
	v_add_f64 v[2:3], v[2:3], v[18:19]
	s_waitcnt vmcnt(9)
	v_add_f64 v[4:5], v[4:5], v[22:23]
	s_waitcnt vmcnt(8)
	v_add_f64 v[2:3], v[2:3], v[24:25]
	s_waitcnt vmcnt(7)
	v_add_f64 v[4:5], v[4:5], v[26:27]
	s_waitcnt vmcnt(6)
	v_add_f64 v[2:3], v[2:3], v[28:29]
	s_waitcnt vmcnt(5)
	v_add_f64 v[4:5], v[4:5], v[30:31]
	s_waitcnt vmcnt(4)
	v_add_f64 v[2:3], v[2:3], v[32:33]
	s_waitcnt vmcnt(3)
	v_add_f64 v[4:5], v[4:5], v[34:35]
	v_div_scale_f64 v[6:7], s[4:5], s[6:7], s[6:7], v[2:3]
	v_div_scale_f64 v[10:11], s[4:5], s[6:7], s[6:7], v[4:5]
	v_rcp_f64_e32 v[12:13], v[6:7]
	v_rcp_f64_e32 v[14:15], v[10:11]
	v_div_scale_f64 v[8:9], vcc, v[2:3], s[6:7], v[2:3]
	v_fma_f64 v[18:19], -v[6:7], v[12:13], 1.0
	v_fma_f64 v[20:21], -v[10:11], v[14:15], 1.0
	v_fmac_f64_e32 v[12:13], v[12:13], v[18:19]
	v_fmac_f64_e32 v[14:15], v[14:15], v[20:21]
	v_fma_f64 v[18:19], -v[6:7], v[12:13], 1.0
	v_fma_f64 v[20:21], -v[10:11], v[14:15], 1.0
	v_fmac_f64_e32 v[12:13], v[12:13], v[18:19]
	v_div_scale_f64 v[16:17], s[4:5], v[4:5], s[6:7], v[4:5]
	v_fmac_f64_e32 v[14:15], v[14:15], v[20:21]
	v_mul_f64 v[18:19], v[8:9], v[12:13]
	v_mul_f64 v[20:21], v[16:17], v[14:15]
	v_fma_f64 v[6:7], -v[6:7], v[18:19], v[8:9]
	v_fma_f64 v[8:9], -v[10:11], v[20:21], v[16:17]
	v_div_fmas_f64 v[6:7], v[6:7], v[12:13], v[18:19]
	s_mov_b64 vcc, s[4:5]
	v_div_fixup_f64 v[2:3], v[6:7], s[6:7], v[2:3]
	v_div_fmas_f64 v[6:7], v[8:9], v[14:15], v[20:21]
	v_div_fixup_f64 v[4:5], v[6:7], s[6:7], v[4:5]
	v_fma_f64 v[4:5], -v[2:3], v[2:3], v[4:5]
	v_cmp_ngt_f64_e32 vcc, 0, v[4:5]
	s_waitcnt vmcnt(2)
	v_cvt_f64_f32_e32 v[8:9], v36
	s_waitcnt vmcnt(0)
	v_cvt_f64_f32_e32 v[10:11], v38
	v_cndmask_b32_e32 v5, 0, v5, vcc
	v_cndmask_b32_e32 v4, 0, v4, vcc
	v_add_f64 v[4:5], v[4:5], s[12:13]
	v_cmp_gt_f64_e32 vcc, s[14:15], v[4:5]
	v_add_f64 v[2:3], v[2:3], 0
	s_nop 0
	v_cndmask_b32_e32 v6, 0, v39, vcc
	v_ldexp_f64 v[4:5], v[4:5], v6
	v_rsq_f64_e32 v[6:7], v[4:5]
	v_cndmask_b32_e32 v16, 0, v40, vcc
	v_cmp_class_f64_e32 vcc, v[4:5], v41
	v_mul_f64 v[12:13], v[4:5], v[6:7]
	v_mul_f64 v[6:7], v[6:7], 0.5
	v_fma_f64 v[14:15], -v[6:7], v[12:13], 0.5
	v_fmac_f64_e32 v[12:13], v[12:13], v[14:15]
	v_fmac_f64_e32 v[6:7], v[6:7], v[14:15]
	v_fma_f64 v[14:15], -v[12:13], v[12:13], v[4:5]
	v_fmac_f64_e32 v[12:13], v[14:15], v[6:7]
	v_fma_f64 v[14:15], -v[12:13], v[12:13], v[4:5]
	v_fmac_f64_e32 v[12:13], v[14:15], v[6:7]
	v_ldexp_f64 v[6:7], v[12:13], v16
	v_cndmask_b32_e32 v5, v7, v5, vcc
	v_cndmask_b32_e32 v4, v6, v4, vcc
	v_div_scale_f64 v[6:7], s[4:5], v[4:5], v[4:5], v[8:9]
	v_rcp_f64_e32 v[12:13], v[6:7]
	v_div_scale_f64 v[14:15], vcc, v[8:9], v[4:5], v[8:9]
	v_fma_f64 v[16:17], -v[6:7], v[12:13], 1.0
	v_fmac_f64_e32 v[12:13], v[12:13], v[16:17]
	v_fma_f64 v[16:17], -v[6:7], v[12:13], 1.0
	v_fmac_f64_e32 v[12:13], v[12:13], v[16:17]
	v_mul_f64 v[16:17], v[14:15], v[12:13]
	v_fma_f64 v[6:7], -v[6:7], v[16:17], v[14:15]
	v_div_fmas_f64 v[6:7], v[6:7], v[12:13], v[16:17]
	v_div_fixup_f64 v[4:5], v[6:7], v[4:5], v[8:9]
	v_cvt_f32_f64_e32 v6, v[4:5]
	v_fma_f64 v[2:3], -v[2:3], v[4:5], v[10:11]
	v_cvt_f32_f64_e32 v2, v[2:3]
	v_mul_f32_e32 v3, v37, v6
	ds_write_b32 v1, v3 offset:18944
	ds_write2st64_b32 v1, v6, v2 offset0:72 offset1:73

.LBB7_8:
	s_load_dwordx2 s[12:13], s[0:1], 0x68
	s_lshl_b32 s17, s6, 5
	s_lshl_b32 s18, s10, 5
	s_sub_i32 s4, s18, s17
	s_ashr_i32 s16, s4, 5
	s_cmp_lt_i32 s16, 1
	v_and_b32_e32 v1, 63, v0
	s_cbranch_scc1 .LBB7_13
	s_load_dwordx8 s[4:11], s[0:1], 0x0
	s_load_dwordx2 s[14:15], s[0:1], 0x20
	v_and_b32_e32 v54, 7, v1
	v_lshlrev_b32_e32 v54, 4, v54
	v_lshrrev_b32_e32 v56, 3, v1
	v_lshlrev_b32_e32 v55, 1, v54
	ds_read_b128 v[2:5], v55 offset:18432
	ds_read_b128 v[6:9], v55 offset:18448
	ds_read_b128 v[10:13], v55 offset:18944
	ds_read_b128 v[14:17], v55 offset:18960
	ds_read_b128 v[18:21], v55 offset:18688
	ds_read_b128 v[22:25], v55 offset:18704
	s_mul_i32 s21, s3, 0x1200
	s_add_i32 s21, s21, 0x4b00
	v_mul_u32_u24_e32 v58, 0x240, v56
	v_add3_u32 v58, v58, v54, s21
	v_and_b32_e32 v59, 31, v1
	v_mul_u32_u24_e32 v59, 0x90, v59
	v_lshrrev_b32_e32 v57, 5, v1
	v_lshlrev_b32_e32 v57, 6, v57
	v_add3_u32 v59, v59, v57, s21
	v_lshlrev_b32_e32 v56, 4, v56
	v_lshlrev_b32_e32 v57, 4, v1
	v_mov_b32_e32 v50, 0
	v_mov_b32_e32 v51, 0
	v_mov_b32_e32 v52, 0
	v_mov_b32_e32 v53, 0
	s_lshl_b32 s20, s17, 2
	s_add_i32 s20, s20, 0x100
	s_mov_b32 s22, 0x3d0880
	s_waitcnt vmcnt(0) lgkmcnt(0)
	v_mov_b32_e32 v26, v104
	v_mov_b32_e32 v27, v105
	v_mov_b32_e32 v28, v106
	v_mov_b32_e32 v29, v107
	v_mov_b32_e32 v30, v108
	v_mov_b32_e32 v31, v109
	v_mov_b32_e32 v32, v110
	v_mov_b32_e32 v33, v111
	v_mov_b32_e32 v38, v112
	v_mov_b32_e32 v39, v113
	v_mov_b32_e32 v40, v114
	v_mov_b32_e32 v41, v115
	v_mov_b32_e32 v34, v100
	v_mov_b32_e32 v35, v101
	v_mov_b32_e32 v36, v102
	v_mov_b32_e32 v37, v103

	.amdhsa_kernel _Z7k_passLILi1ELi0ELi1EEvPKiS1_PKfPKtS5_S3_S3_S3_S3_S3_S3_PK15HIP_vector_typeIjLj4EEPKdPdS1_PtS1_
		.amdhsa_group_segment_fixed_size 37632
		.amdhsa_private_segment_fixed_size 0
		.amdhsa_kernarg_size 392
		.amdhsa_user_sgpr_count 2
		.amdhsa_user_sgpr_dispatch_ptr 0
		.amdhsa_user_sgpr_queue_ptr 0
		.amdhsa_user_sgpr_kernarg_segment_ptr 1
		.amdhsa_user_sgpr_dispatch_id 0
		.amdhsa_user_sgpr_kernarg_preload_length 0
		.amdhsa_user_sgpr_kernarg_preload_offset 0
		.amdhsa_user_sgpr_private_segment_size 0
		.amdhsa_uses_dynamic_stack 0
		.amdhsa_enable_private_segment 0
		.amdhsa_system_sgpr_workgroup_id_x 1
		.amdhsa_system_sgpr_workgroup_id_y 0
		.amdhsa_system_sgpr_workgroup_id_z 0
		.amdhsa_system_sgpr_workgroup_info 0
		.amdhsa_system_vgpr_workitem_id 0
		.amdhsa_next_free_vgpr 128
		.amdhsa_next_free_sgpr 56
		.amdhsa_accum_offset 128
		.amdhsa_reserve_vcc 1
		.amdhsa_float_round_mode_32 0
		.amdhsa_float_round_mode_16_64 0
		.amdhsa_float_denorm_mode_32 3
		.amdhsa_float_denorm_mode_16_64 3
		.amdhsa_dx10_clamp 1
		.amdhsa_ieee_mode 1
		.amdhsa_fp16_overflow 0
		.amdhsa_tg_split 0
		.amdhsa_exception_fp_ieee_invalid_op 0
		.amdhsa_exception_fp_denorm_src 0
		.amdhsa_exception_fp_ieee_div_zero 0
		.amdhsa_exception_fp_ieee_overflow 0
		.amdhsa_exception_fp_ieee_underflow 0
		.amdhsa_exception_fp_ieee_inexact 0
		.amdhsa_exception_int_div_zero 0
	.end_amdhsa_kernel

_Z8k_passCUILi1EEvPKiS1_PKfPKtS5_S3_S3_S3_S3_S3_S3_PK15HIP_vector_typeIjLj4EES9_S9_PKdSB_S1_S1_S5_S3_PtPd:
	s_load_dwordx4 s[4:7], s[0:1], 0x58
	s_load_dwordx2 s[8:9], s[0:1], 0x68
	s_load_dword s50, s[0:1], 0xb0
	s_load_dwordx2 s[52:53], s[0:1], 0x80
	s_load_dwordx4 s[56:59], s[0:1], 0x0
	s_load_dwordx2 s[60:61], s[0:1], 0x10
	v_mov_b32_e32 v3, 0
	v_lshlrev_b32_e32 v2, 4, v0
	s_movk_i32 s3, 0x2000
	s_waitcnt lgkmcnt(0)
	v_readfirstlane_b32 s54, v0
	v_lshrrev_b32_e32 v82, 3, v0
	v_and_b32_e32 v82, 7, v82
	v_lshlrev_b32_e32 v82, 4, v82
	s_lshr_b32 s54, s54, 6
	s_mul_i32 s55, s50, s54
	s_add_i32 s55, s55, s2
	s_min_u32 s55, s55, 0xc34
	s_lshl_b32 s55, s55, 7
	s_add_u32 s52, s52, s55
	s_addc_u32 s53, s53, 0
	s_load_dword s62, s[52:53], 0x0
	s_load_dword s64, s[52:53], 0x80
	v_lshl_add_u64 v[16:17], s[6:7], 0, v[2:3]
	global_load_dwordx4 v[4:7], v2, s[4:5]
	global_load_dwordx4 v[8:11], v2, s[6:7]
	global_load_dwordx4 v[12:15], v2, s[8:9]
	v_add_co_u32_e32 v16, vcc, s3, v16
	v_lshl_add_u64 v[20:21], s[8:9], 0, v[2:3]
	s_nop 0
	v_addc_co_u32_e32 v17, vcc, 0, v17, vcc
	v_add_co_u32_e32 v20, vcc, 0x2000, v20
	global_load_dwordx4 v[16:19], v[16:17], off
	s_nop 0
	v_addc_co_u32_e32 v21, vcc, 0, v21, vcc
	global_load_dwordx4 v[20:23], v[20:21], off
	s_mov_b32 s28, 0
	v_readfirstlane_b32 s3, v0
	v_cmp_gt_u32_e32 vcc, 64, v0
	s_waitcnt vmcnt(4)
	ds_write_b128 v2, v[4:7]
	s_waitcnt vmcnt(3)
	ds_write_b128 v2, v[8:11] offset:16384
	s_waitcnt vmcnt(2)
	ds_write_b128 v2, v[12:15] offset:32768
	s_waitcnt vmcnt(1)
	ds_write_b128 v2, v[16:19] offset:24576
	s_waitcnt vmcnt(0)
	ds_write_b128 v2, v[20:23] offset:40960
	s_waitcnt lgkmcnt(0)
	s_lshl_b32 s63, s62, 2
	v_add_u32_e32 v83, s63, v82
	global_load_dwordx4 v[70:73], v83, s[56:57]
	global_load_dwordx4 v[74:77], v83, s[58:59]
	global_load_dwordx4 v[78:81], v83, s[60:61]
	s_and_saveexec_b64 s[20:21], vcc
	s_cbranch_execz .LBB8_2
	s_load_dwordx4 s[4:7], s[0:1], 0x70
	s_load_dwordx4 s[16:19], s[0:1], 0x48
	v_lshlrev_b32_e32 v2, 3, v0
	s_load_dwordx8 s[8:15], s[0:1], 0x28
	v_lshlrev_b32_e32 v1, 2, v0
	s_waitcnt lgkmcnt(0)
	global_load_dwordx2 v[4:5], v2, s[4:5]
	global_load_dwordx2 v[6:7], v2, s[4:5] offset:512
	global_load_dwordx2 v[8:9], v2, s[4:5] offset:1024
	global_load_dwordx2 v[10:11], v2, s[4:5] offset:1536
	global_load_dwordx2 v[12:13], v2, s[4:5] offset:2048
	global_load_dwordx2 v[14:15], v2, s[4:5] offset:2560
	global_load_dwordx2 v[16:17], v2, s[4:5] offset:3072
	global_load_dwordx2 v[18:19], v2, s[4:5] offset:3584
	v_lshl_add_u64 v[20:21], s[4:5], 0, v[2:3]
	s_movk_i32 s4, 0x1000
	v_add_co_u32_e32 v36, vcc, s4, v20
	s_mov_b32 s24, 0
	s_nop 0
	v_addc_co_u32_e32 v37, vcc, 0, v21, vcc
	global_load_dwordx2 v[20:21], v[36:37], off
	global_load_dwordx2 v[22:23], v[36:37], off offset:512
	global_load_dwordx2 v[24:25], v[36:37], off offset:1024
	global_load_dwordx2 v[26:27], v[36:37], off offset:1536
	global_load_dwordx2 v[28:29], v[36:37], off offset:2048
	global_load_dwordx2 v[30:31], v[36:37], off offset:2560
	global_load_dwordx2 v[32:33], v[36:37], off offset:3072
	global_load_dwordx2 v[34:35], v[36:37], off offset:3584
	global_load_dword v67, v1, s[10:11]
	global_load_dword v68, v1, s[12:13]
	global_load_dwordx2 v[38:39], v2, s[6:7] offset:512
	global_load_dwordx2 v[40:41], v2, s[6:7]
	global_load_dwordx2 v[42:43], v2, s[6:7] offset:1536
	global_load_dwordx2 v[44:45], v2, s[6:7] offset:1024
	global_load_dwordx2 v[46:47], v2, s[6:7] offset:2560
	global_load_dwordx2 v[48:49], v2, s[6:7] offset:2048
	global_load_dwordx2 v[50:51], v2, s[6:7] offset:3584
	global_load_dwordx2 v[52:53], v2, s[6:7] offset:3072
	v_lshl_add_u64 v[36:37], s[6:7], 0, v[2:3]
	v_add_co_u32_e32 v2, vcc, s4, v36
	s_mov_b32 s25, 0x412e8480
	s_nop 0
	v_addc_co_u32_e32 v3, vcc, 0, v37, vcc
	global_load_dwordx2 v[36:37], v[2:3], off
	global_load_dwordx2 v[54:55], v[2:3], off offset:512
	global_load_dwordx2 v[56:57], v[2:3], off offset:1024
	global_load_dwordx2 v[58:59], v[2:3], off offset:1536
	global_load_dwordx2 v[60:61], v[2:3], off offset:2048
	global_load_dwordx2 v[62:63], v[2:3], off offset:2560
	global_load_dwordx2 v[64:65], v[2:3], off offset:3072
	s_nop 0
	global_load_dwordx2 v[2:3], v[2:3], off offset:3584
	s_mov_b32 s22, 0x88e368f1
	s_mov_b32 s23, 0x3ee4f8b5
	s_mov_b32 s26, 0
	s_brev_b32 s27, 8
	v_mov_b32_e32 v66, 0x100
	s_waitcnt vmcnt(33)
	v_add_f64 v[4:5], v[4:5], 0
	s_waitcnt vmcnt(32)
	v_add_f64 v[6:7], v[6:7], 0
	s_waitcnt vmcnt(31)
	v_add_f64 v[4:5], v[4:5], v[8:9]
	s_waitcnt vmcnt(30)
	v_add_f64 v[6:7], v[6:7], v[10:11]
	s_waitcnt vmcnt(29)
	v_add_f64 v[4:5], v[4:5], v[12:13]
	s_waitcnt vmcnt(28)
	v_add_f64 v[6:7], v[6:7], v[14:15]
	s_waitcnt vmcnt(27)
	v_add_f64 v[4:5], v[4:5], v[16:17]
	s_waitcnt vmcnt(26)
	v_add_f64 v[6:7], v[6:7], v[18:19]
	s_waitcnt vmcnt(25)
	v_add_f64 v[4:5], v[4:5], v[20:21]
	s_waitcnt vmcnt(24)
	v_add_f64 v[6:7], v[6:7], v[22:23]
	s_waitcnt vmcnt(23)
	v_add_f64 v[4:5], v[4:5], v[24:25]
	s_waitcnt vmcnt(22)
	v_add_f64 v[6:7], v[6:7], v[26:27]
	s_waitcnt vmcnt(21)
	v_add_f64 v[4:5], v[4:5], v[28:29]
	s_waitcnt vmcnt(20)
	v_add_f64 v[6:7], v[6:7], v[30:31]
	s_waitcnt vmcnt(19)
	v_add_f64 v[4:5], v[4:5], v[32:33]
	s_waitcnt vmcnt(18)
	v_add_f64 v[6:7], v[6:7], v[34:35]
	v_div_scale_f64 v[8:9], s[4:5], s[24:25], s[24:25], v[4:5]
	v_div_scale_f64 v[12:13], s[4:5], s[24:25], s[24:25], v[6:7]
	v_rcp_f64_e32 v[14:15], v[8:9]
	v_rcp_f64_e32 v[16:17], v[12:13]
	v_div_scale_f64 v[10:11], vcc, v[4:5], s[24:25], v[4:5]
	v_fma_f64 v[20:21], -v[8:9], v[14:15], 1.0
	v_fma_f64 v[22:23], -v[12:13], v[16:17], 1.0
	v_fmac_f64_e32 v[14:15], v[14:15], v[20:21]
	v_fmac_f64_e32 v[16:17], v[16:17], v[22:23]
	v_fma_f64 v[20:21], -v[8:9], v[14:15], 1.0
	v_fma_f64 v[22:23], -v[12:13], v[16:17], 1.0
	v_fmac_f64_e32 v[14:15], v[14:15], v[20:21]
	v_div_scale_f64 v[18:19], s[4:5], v[6:7], s[24:25], v[6:7]
	v_fmac_f64_e32 v[16:17], v[16:17], v[22:23]
	v_mul_f64 v[20:21], v[10:11], v[14:15]
	v_mul_f64 v[22:23], v[18:19], v[16:17]
	v_fma_f64 v[8:9], -v[8:9], v[20:21], v[10:11]
	v_fma_f64 v[10:11], -v[12:13], v[22:23], v[18:19]
	v_div_fmas_f64 v[8:9], v[8:9], v[14:15], v[20:21]
	s_mov_b64 vcc, s[4:5]
	v_div_fixup_f64 v[4:5], v[8:9], s[24:25], v[4:5]
	v_div_fmas_f64 v[8:9], v[10:11], v[16:17], v[22:23]
	v_div_fixup_f64 v[6:7], v[8:9], s[24:25], v[6:7]
	v_fma_f64 v[6:7], -v[4:5], v[4:5], v[6:7]
	v_cmp_ngt_f64_e32 vcc, 0, v[6:7]
	global_load_dword v22, v1, s[8:9]
	global_load_dword v23, v1, s[14:15]
	global_load_dword v24, v1, s[16:17]
	global_load_dword v25, v1, s[18:19]
	v_cndmask_b32_e32 v7, 0, v7, vcc
	v_cndmask_b32_e32 v6, 0, v6, vcc
	v_add_f64 v[6:7], v[6:7], s[22:23]
	v_cmp_gt_f64_e32 vcc, s[26:27], v[6:7]
	v_mov_b32_e32 v26, 0xffffff80
	v_mov_b32_e32 v27, 0x260
	v_cndmask_b32_e32 v8, 0, v66, vcc
	v_ldexp_f64 v[6:7], v[6:7], v8
	v_rsq_f64_e32 v[8:9], v[6:7]
	s_waitcnt vmcnt(21)
	v_cvt_f64_f32_e32 v[10:11], v67
	v_add_f64 v[4:5], v[4:5], 0
	v_mul_f64 v[12:13], v[6:7], v[8:9]
	v_mul_f64 v[8:9], v[8:9], 0.5
	v_fma_f64 v[14:15], -v[8:9], v[12:13], 0.5
	v_fmac_f64_e32 v[12:13], v[12:13], v[14:15]
	v_fmac_f64_e32 v[8:9], v[8:9], v[14:15]
	v_fma_f64 v[14:15], -v[12:13], v[12:13], v[6:7]
	v_fmac_f64_e32 v[12:13], v[14:15], v[8:9]
	v_fma_f64 v[14:15], -v[12:13], v[12:13], v[6:7]
	v_fmac_f64_e32 v[12:13], v[14:15], v[8:9]
	v_cndmask_b32_e32 v8, 0, v26, vcc
	v_ldexp_f64 v[8:9], v[12:13], v8
	v_cmp_class_f64_e32 vcc, v[6:7], v27
	s_nop 1
	v_cndmask_b32_e32 v7, v9, v7, vcc
	v_cndmask_b32_e32 v6, v8, v6, vcc
	v_div_scale_f64 v[8:9], s[4:5], v[6:7], v[6:7], v[10:11]
	v_rcp_f64_e32 v[12:13], v[8:9]
	s_nop 0
	v_fma_f64 v[14:15], -v[8:9], v[12:13], 1.0
	v_fmac_f64_e32 v[12:13], v[12:13], v[14:15]
	v_fma_f64 v[14:15], -v[8:9], v[12:13], 1.0
	v_fmac_f64_e32 v[12:13], v[12:13], v[14:15]
	v_div_scale_f64 v[14:15], vcc, v[10:11], v[6:7], v[10:11]
	v_mul_f64 v[16:17], v[14:15], v[12:13]
	v_fma_f64 v[8:9], -v[8:9], v[16:17], v[14:15]
	s_nop 1
	v_div_fmas_f64 v[8:9], v[8:9], v[12:13], v[16:17]
	v_div_fixup_f64 v[6:7], v[8:9], v[6:7], v[10:11]
	s_waitcnt vmcnt(18)
	v_add_f64 v[10:11], v[40:41], 0
	s_waitcnt vmcnt(16)
	v_add_f64 v[10:11], v[10:11], v[44:45]
	s_waitcnt vmcnt(14)
	v_add_f64 v[10:11], v[10:11], v[48:49]
	s_waitcnt vmcnt(12)
	v_add_f64 v[10:11], v[10:11], v[52:53]
	s_waitcnt vmcnt(11)
	v_add_f64 v[10:11], v[10:11], v[36:37]
	s_waitcnt vmcnt(9)
	v_add_f64 v[10:11], v[10:11], v[56:57]
	v_add_f64 v[12:13], v[38:39], 0
	s_waitcnt vmcnt(7)
	v_add_f64 v[10:11], v[10:11], v[60:61]
	v_add_f64 v[12:13], v[12:13], v[42:43]
	s_waitcnt vmcnt(5)
	v_add_f64 v[10:11], v[10:11], v[64:65]
	v_add_f64 v[12:13], v[12:13], v[46:47]
	v_div_scale_f64 v[14:15], s[4:5], s[24:25], s[24:25], v[10:11]
	v_add_f64 v[12:13], v[12:13], v[50:51]
	v_rcp_f64_e32 v[16:17], v[14:15]
	v_add_f64 v[12:13], v[12:13], v[54:55]
	v_add_f64 v[12:13], v[12:13], v[58:59]
	v_add_f64 v[12:13], v[12:13], v[62:63]
	s_waitcnt vmcnt(4)
	v_add_f64 v[2:3], v[12:13], v[2:3]
	v_fma_f64 v[12:13], -v[14:15], v[16:17], 1.0
	v_fmac_f64_e32 v[16:17], v[16:17], v[12:13]
	v_fma_f64 v[12:13], -v[14:15], v[16:17], 1.0
	v_fmac_f64_e32 v[16:17], v[16:17], v[12:13]
	v_div_scale_f64 v[12:13], vcc, v[10:11], s[24:25], v[10:11]
	v_mul_f64 v[18:19], v[12:13], v[16:17]
	v_fma_f64 v[12:13], -v[14:15], v[18:19], v[12:13]
	v_div_scale_f64 v[14:15], s[4:5], s[24:25], s[24:25], v[2:3]
	v_rcp_f64_e32 v[20:21], v[14:15]
	v_div_fmas_f64 v[12:13], v[12:13], v[16:17], v[18:19]
	v_div_fixup_f64 v[10:11], v[12:13], s[24:25], v[10:11]
	v_cvt_f64_f32_e32 v[8:9], v68
	v_fma_f64 v[12:13], -v[14:15], v[20:21], 1.0
	v_fmac_f64_e32 v[20:21], v[20:21], v[12:13]
	v_fma_f64 v[12:13], -v[14:15], v[20:21], 1.0
	v_fmac_f64_e32 v[20:21], v[20:21], v[12:13]
	v_div_scale_f64 v[12:13], vcc, v[2:3], s[24:25], v[2:3]
	v_mul_f64 v[16:17], v[12:13], v[20:21]
	v_fma_f64 v[12:13], -v[14:15], v[16:17], v[12:13]
	v_cvt_f32_f64_e32 v28, v[6:7]
	s_nop 0
	v_div_fmas_f64 v[12:13], v[12:13], v[20:21], v[16:17]
	v_div_fixup_f64 v[2:3], v[12:13], s[24:25], v[2:3]
	v_fma_f64 v[2:3], -v[10:11], v[10:11], v[2:3]
	v_cmp_ngt_f64_e32 vcc, 0, v[2:3]
	v_fma_f64 v[4:5], -v[4:5], v[6:7], v[8:9]
	v_cvt_f32_f64_e32 v16, v[4:5]
	v_cndmask_b32_e32 v3, 0, v3, vcc
	v_cndmask_b32_e32 v2, 0, v2, vcc
	v_add_f64 v[2:3], v[2:3], s[22:23]
	v_cmp_gt_f64_e32 vcc, s[26:27], v[2:3]
	s_waitcnt vmcnt(1)
	v_cvt_f64_f32_e32 v[4:5], v24
	ds_write2st64_b32 v1, v28, v16 offset0:208 offset1:209
	v_cndmask_b32_e32 v12, 0, v66, vcc
	v_ldexp_f64 v[2:3], v[2:3], v12
	v_rsq_f64_e32 v[12:13], v[2:3]
	v_mul_f32_e32 v18, v22, v28
	v_mul_f64 v[6:7], v[2:3], v[12:13]
	v_mul_f64 v[8:9], v[12:13], 0.5
	v_fma_f64 v[12:13], -v[8:9], v[6:7], 0.5
	v_fmac_f64_e32 v[6:7], v[6:7], v[12:13]
	v_fma_f64 v[14:15], -v[6:7], v[6:7], v[2:3]
	v_fmac_f64_e32 v[8:9], v[8:9], v[12:13]
	v_fmac_f64_e32 v[6:7], v[14:15], v[8:9]
	v_fma_f64 v[12:13], -v[6:7], v[6:7], v[2:3]
	v_fmac_f64_e32 v[6:7], v[12:13], v[8:9]
	v_cndmask_b32_e32 v8, 0, v26, vcc
	v_ldexp_f64 v[6:7], v[6:7], v8
	v_cmp_class_f64_e32 vcc, v[2:3], v27
	v_cvt_f64_f32_e32 v[12:13], v23
	s_nop 0
	v_cndmask_b32_e32 v3, v7, v3, vcc
	v_cndmask_b32_e32 v2, v6, v2, vcc
	v_div_scale_f64 v[6:7], s[4:5], v[2:3], v[2:3], v[4:5]
	v_rcp_f64_e32 v[8:9], v[6:7]
	s_nop 0
	v_fma_f64 v[14:15], -v[6:7], v[8:9], 1.0
	v_fmac_f64_e32 v[8:9], v[8:9], v[14:15]
	v_fma_f64 v[14:15], -v[6:7], v[8:9], 1.0
	v_fmac_f64_e32 v[8:9], v[8:9], v[14:15]
	v_div_scale_f64 v[14:15], vcc, v[4:5], v[2:3], v[4:5]
	v_mul_f64 v[16:17], v[14:15], v[8:9]
	v_fma_f64 v[6:7], -v[6:7], v[16:17], v[14:15]
	s_nop 1
	v_div_fmas_f64 v[6:7], v[6:7], v[8:9], v[16:17]
	v_div_fixup_f64 v[2:3], v[6:7], v[2:3], v[4:5]
	s_waitcnt vmcnt(0)
	v_cvt_f64_f32_e32 v[4:5], v25
	v_add_f64 v[6:7], v[10:11], v[12:13]
	v_cvt_f32_f64_e32 v8, v[2:3]
	v_fma_f64 v[2:3], -v[6:7], v[2:3], v[4:5]
	v_cvt_f32_f64_e32 v2, v[2:3]
	v_fmac_f32_e32 v2, v23, v8
	ds_write2st64_b32 v1, v18, v8 offset0:210 offset1:211
	ds_write_b32 v1, v2 offset:54272
.LBB8_2:
	s_or_b64 exec, exec, s[20:21]
	s_waitcnt lgkmcnt(0)
	s_barrier
	s_load_dword s4, s[0:1], 0xb0
	v_and_b32_e32 v98, 31, v0
	v_lshlrev_b32_e32 v1, 3, v98
	s_lshr_b32 s3, s3, 6
	v_add_u32_e32 v1, 0xd000, v1
	ds_read2_b64 v[66:69], v1 offset0:96 offset1:128
	s_waitcnt lgkmcnt(0)
	s_mul_i32 s4, s4, s3
	s_add_i32 s4, s4, s2
	s_lshl_b32 s14, s4, 5
	s_cmpk_lt_i32 s4, 0xc35
	s_cselect_b64 s[16:17], -1, 0
	s_cmpk_gt_i32 s4, 0xc34
	s_mov_b32 s20, 0
	s_cbranch_scc1 .LBB8_4
	s_mov_b32 s20, s62
	s_mov_b32 s28, s64
.LBB8_4:
	s_load_dwordx2 s[12:13], s[0:1], 0xa8
	s_load_dwordx2 s[18:19], s[0:1], 0x98
	s_waitcnt lgkmcnt(0)
	s_sub_i32 s4, s28, s20
	s_add_i32 s4, s4, 31
	v_and_b32_e32 v1, 63, v0
	s_ashr_i32 s15, s4, 5
	s_cmp_lt_i32 s15, 1
	v_or_b32_e32 v90, s14, v98
	v_and_b32_e32 v100, 32, v0
	v_lshlrev_b32_e32 v99, 4, v1
	s_cbranch_scc1 .LBB8_7
	s_load_dwordx8 s[4:11], s[0:1], 0x0
	s_load_dwordx2 s[24:25], s[0:1], 0x20
	s_load_dwordx2 s[30:31], s[0:1], 0x80
	v_and_b32_e32 v34, 7, v1
	v_lshlrev_b32_e32 v34, 4, v34
	v_lshrrev_b32_e32 v35, 3, v1
	s_lshl_b32 s32, s3, 12
	s_add_i32 s33, s32, 0x2000
	s_add_i32 s32, s32, 0xb500
	s_cmp_lt_u32 s3, 2
	s_cselect_b32 s32, s33, s32
	v_lshlrev_b32_e32 v36, 1, v35
	v_and_b32_e32 v36, 7, v36
	v_or_b32_e32 v37, 1, v36
	v_lshlrev_b32_e32 v36, 4, v36
	v_lshlrev_b32_e32 v37, 4, v37
	v_xor_b32_e32 v36, v36, v34
	v_xor_b32_e32 v37, v37, v34
	v_lshl_add_u32 v39, v35, 9, s32
	v_add_u32_e32 v36, v36, v39
	v_add_u32_e32 v37, v37, v39
	v_lshrrev_b32_e32 v38, 1, v98
	v_and_b32_e32 v38, 7, v38
	v_lshrrev_b32_e32 v39, 3, v100
	v_xor_b32_e32 v38, v38, v39
	v_lshlrev_b32_e32 v38, 4, v38
	v_lshl_add_u32 v39, v98, 7, s32
	v_add_u32_e32 v38, v38, v39
	v_lshlrev_b32_e32 v35, 4, v35
	s_mov_b32 s35, 0x1869f
	v_mov_b32_e32 v2, 0
	v_mov_b32_e32 v3, 0
	v_mov_b32_e32 v4, 0
	v_mov_b32_e32 v5, 0
	v_mov_b32_e32 v6, 0
	v_mov_b32_e32 v7, 0
	v_mov_b32_e32 v8, 0
	v_mov_b32_e32 v9, 0
	v_mov_b32_e32 v10, 0
	v_mov_b32_e32 v11, 0
	v_mov_b32_e32 v12, 0
	v_mov_b32_e32 v13, 0
	v_mov_b32_e32 v14, 0
	v_mov_b32_e32 v15, 0
	v_mov_b32_e32 v16, 0
	v_mov_b32_e32 v17, 0
	v_mov_b32_e32 v18, 0
	v_mov_b32_e32 v19, 0
	v_mov_b32_e32 v20, 0
	v_mov_b32_e32 v21, 0
	v_mov_b32_e32 v22, 0
	v_mov_b32_e32 v23, 0
	v_mov_b32_e32 v24, 0
	v_mov_b32_e32 v25, 0
	v_mov_b32_e32 v26, 0
	v_mov_b32_e32 v27, 0
	v_mov_b32_e32 v28, 0
	v_mov_b32_e32 v29, 0
	v_mov_b32_e32 v30, 0
	v_mov_b32_e32 v31, 0
	v_mov_b32_e32 v32, 0
	v_mov_b32_e32 v33, 0
	s_waitcnt vmcnt(0) lgkmcnt(0)
	v_mov_b32_e32 v42, v70
	v_mov_b32_e32 v43, v71
	v_mov_b32_e32 v44, v72
	v_mov_b32_e32 v45, v73
	v_mov_b32_e32 v46, v74
	v_mov_b32_e32 v47, v75
	v_mov_b32_e32 v48, v76
	v_mov_b32_e32 v49, v77
	v_mov_b32_e32 v50, v78
	v_mov_b32_e32 v51, v79
	v_mov_b32_e32 v52, v80
	v_mov_b32_e32 v53, v81
	v_lshlrev_b32_e32 v39, 2, v90
	global_load_dword v40, v39, s[30:31]
	global_load_dword v41, v39, s[30:31] offset:4
	s_lshl_b32 s34, s20, 2
	v_min_u32_e32 v42, s35, v42
	v_min_u32_e32 v46, s35, v46
	v_min_u32_e32 v43, s35, v43
	v_min_u32_e32 v47, s35, v47
	v_min_u32_e32 v44, s35, v44
	v_min_u32_e32 v48, s35, v48
	v_min_u32_e32 v45, s35, v45
	v_min_u32_e32 v49, s35, v49
	v_lshl_or_b32 v42, v42, 7, v34
	v_lshl_or_b32 v46, v46, 7, v34
	v_lshl_or_b32 v43, v43, 7, v34
	v_lshl_or_b32 v47, v47, 7, v34
	v_lshl_or_b32 v44, v44, 7, v34
	v_lshl_or_b32 v48, v48, 7, v34
	v_lshl_or_b32 v45, v45, 7, v34
	v_lshl_or_b32 v49, v49, 7, v34
	global_load_dwordx4 v[70:73], v42, s[24:25]
	global_load_dwordx4 v[74:77], v43, s[24:25]
	global_load_dwordx4 v[78:81], v44, s[24:25]
	global_load_dwordx4 v[82:85], v45, s[24:25]
	global_load_dwordx4 v[86:89], v46, s[10:11]
	global_load_dwordx4 v[90:93], v47, s[10:11]
	global_load_dwordx4 v[94:97], v48, s[10:11]
	global_load_dwordx4 v[102:105], v49, s[10:11]
	s_add_i32 s34, s34, 0x80
	v_add_u32_e32 v39, s34, v35
	global_load_dwordx4 v[42:45], v39, s[4:5]
	global_load_dwordx4 v[46:49], v39, s[6:7]
.Lcu_loop:
	s_waitcnt vmcnt(2)
	s_sub_i32 s36, s28, s20
	s_cmp_ge_i32 s36, 32
	s_cbranch_scc1 .Lcu_noclampe
	v_lshrrev_b32_e32 v39, 2, v35
	v_sub_u32_e32 v39, s36, v39
	v_cmp_gt_i32_e64 s[40:41], v39, 0
	v_cmp_gt_i32_e64 s[42:43], v39, 1
	v_cmp_gt_i32_e64 s[44:45], v39, 2
	v_cmp_gt_i32_e64 s[46:47], v39, 3
	v_cndmask_b32_e64 v50, 0, v50, s[40:41]
	v_cndmask_b32_e64 v51, 0, v51, s[42:43]
	v_cndmask_b32_e64 v52, 0, v52, s[44:45]
	v_cndmask_b32_e64 v53, 0, v53, s[46:47]
.Lcu_noclampe:
	v_lshlrev_b32_e32 v39, 1, v34
	ds_read_b128 v[112:115], v39 offset:53248
	ds_read_b128 v[116:119], v39 offset:53760
	ds_read_b128 v[120:123], v39 offset:53504
	s_waitcnt lgkmcnt(0)
	v_lshlrev_b32_e32 v124, 16, v86
	v_and_b32_e32 v125, 0xffff0000, v86
	v_lshlrev_b32_e32 v126, 16, v70
	v_and_b32_e32 v127, 0xffff0000, v70
	v_add_f32_e32 v124, v126, v124
	v_add_f32_e32 v125, v127, v125
	v_fma_f32 v126, v116, v50, v120
	v_fma_f32 v127, v117, v50, v121
	v_fmac_f32_e32 v126, v112, v124
	v_fmac_f32_e32 v127, v113, v125
	v_max_f32_e32 v126, 0, v126
	v_max_f32_e32 v127, 0, v127
	v_cvt_pk_f16_f32 v54, v126, v127
	v_lshlrev_b32_e32 v106, 16, v87
	v_and_b32_e32 v107, 0xffff0000, v87
	v_lshlrev_b32_e32 v108, 16, v71
	v_and_b32_e32 v109, 0xffff0000, v71
	v_add_f32_e32 v106, v108, v106
	v_add_f32_e32 v107, v109, v107
	v_fma_f32 v108, v118, v50, v122
	v_fma_f32 v109, v119, v50, v123
	v_fmac_f32_e32 v108, v114, v106
	v_fmac_f32_e32 v109, v115, v107
	v_max_f32_e32 v108, 0, v108
	v_max_f32_e32 v109, 0, v109
	v_cvt_pk_f16_f32 v55, v108, v109
	ds_write_b64 v36, v[54:55] offset:0
	v_lshlrev_b32_e32 v124, 16, v90
	v_and_b32_e32 v125, 0xffff0000, v90
	v_lshlrev_b32_e32 v126, 16, v74
	v_and_b32_e32 v127, 0xffff0000, v74
	v_add_f32_e32 v124, v126, v124
	v_add_f32_e32 v125, v127, v125
	v_fma_f32 v126, v116, v51, v120
	v_fma_f32 v127, v117, v51, v121
	v_fmac_f32_e32 v126, v112, v124
	v_fmac_f32_e32 v127, v113, v125
	v_max_f32_e32 v126, 0, v126
	v_max_f32_e32 v127, 0, v127
	v_cvt_pk_f16_f32 v56, v126, v127
	v_lshlrev_b32_e32 v106, 16, v91
	v_and_b32_e32 v107, 0xffff0000, v91
	v_lshlrev_b32_e32 v108, 16, v75
	v_and_b32_e32 v109, 0xffff0000, v75
	v_add_f32_e32 v106, v108, v106
	v_add_f32_e32 v107, v109, v107
	v_fma_f32 v108, v118, v51, v122
	v_fma_f32 v109, v119, v51, v123
	v_fmac_f32_e32 v108, v114, v106
	v_fmac_f32_e32 v109, v115, v107
	v_max_f32_e32 v108, 0, v108
	v_max_f32_e32 v109, 0, v109
	v_cvt_pk_f16_f32 v57, v108, v109
	ds_write_b64 v36, v[56:57] offset:128
	v_lshlrev_b32_e32 v124, 16, v94
	v_and_b32_e32 v125, 0xffff0000, v94
	v_lshlrev_b32_e32 v126, 16, v78
	v_and_b32_e32 v127, 0xffff0000, v78
	v_add_f32_e32 v124, v126, v124
	v_add_f32_e32 v125, v127, v125
	v_fma_f32 v126, v116, v52, v120
	v_fma_f32 v127, v117, v52, v121
	v_fmac_f32_e32 v126, v112, v124
	v_fmac_f32_e32 v127, v113, v125
	v_max_f32_e32 v126, 0, v126
	v_max_f32_e32 v127, 0, v127
	v_cvt_pk_f16_f32 v54, v126, v127
	v_lshlrev_b32_e32 v106, 16, v95
	v_and_b32_e32 v107, 0xffff0000, v95
	v_lshlrev_b32_e32 v108, 16, v79
	v_and_b32_e32 v109, 0xffff0000, v79
	v_add_f32_e32 v106, v108, v106
	v_add_f32_e32 v107, v109, v107
	v_fma_f32 v108, v118, v52, v122
	v_fma_f32 v109, v119, v52, v123
	v_fmac_f32_e32 v108, v114, v106
	v_fmac_f32_e32 v109, v115, v107
	v_max_f32_e32 v108, 0, v108
	v_max_f32_e32 v109, 0, v109
	v_cvt_pk_f16_f32 v55, v108, v109
	ds_write_b64 v37, v[54:55] offset:256
	v_lshlrev_b32_e32 v124, 16, v102
	v_and_b32_e32 v125, 0xffff0000, v102
	v_lshlrev_b32_e32 v126, 16, v82
	v_and_b32_e32 v127, 0xffff0000, v82
	v_add_f32_e32 v124, v126, v124
	v_add_f32_e32 v125, v127, v125
	v_fma_f32 v126, v116, v53, v120
	v_fma_f32 v127, v117, v53, v121
	v_fmac_f32_e32 v126, v112, v124
	v_fmac_f32_e32 v127, v113, v125
	v_max_f32_e32 v126, 0, v126
	v_max_f32_e32 v127, 0, v127
	v_cvt_pk_f16_f32 v56, v126, v127
	v_lshlrev_b32_e32 v106, 16, v103
	v_and_b32_e32 v107, 0xffff0000, v103
	v_lshlrev_b32_e32 v108, 16, v83
	v_and_b32_e32 v109, 0xffff0000, v83
	v_add_f32_e32 v106, v108, v106
	v_add_f32_e32 v107, v109, v107
	v_fma_f32 v108, v118, v53, v122
	v_fma_f32 v109, v119, v53, v123
	v_fmac_f32_e32 v108, v114, v106
	v_fmac_f32_e32 v109, v115, v107
	v_max_f32_e32 v108, 0, v108
	v_max_f32_e32 v109, 0, v109
	v_cvt_pk_f16_f32 v57, v108, v109
	ds_write_b64 v37, v[56:57] offset:384
	ds_read_b128 v[112:115], v39 offset:53264
	ds_read_b128 v[116:119], v39 offset:53776
	ds_read_b128 v[120:123], v39 offset:53520
	s_waitcnt lgkmcnt(0)
	v_lshlrev_b32_e32 v124, 16, v88
	v_and_b32_e32 v125, 0xffff0000, v88
	v_lshlrev_b32_e32 v126, 16, v72
	v_and_b32_e32 v127, 0xffff0000, v72
	v_add_f32_e32 v124, v126, v124
	v_add_f32_e32 v125, v127, v125
	v_fma_f32 v126, v116, v50, v120
	v_fma_f32 v127, v117, v50, v121
	v_fmac_f32_e32 v126, v112, v124
	v_fmac_f32_e32 v127, v113, v125
	v_max_f32_e32 v126, 0, v126
	v_max_f32_e32 v127, 0, v127
	v_cvt_pk_f16_f32 v54, v126, v127
	v_lshlrev_b32_e32 v106, 16, v89
	v_and_b32_e32 v107, 0xffff0000, v89
	v_lshlrev_b32_e32 v108, 16, v73
	v_and_b32_e32 v109, 0xffff0000, v73
	v_add_f32_e32 v106, v108, v106
	v_add_f32_e32 v107, v109, v107
	v_fma_f32 v108, v118, v50, v122
	v_fma_f32 v109, v119, v50, v123
	v_fmac_f32_e32 v108, v114, v106
	v_fmac_f32_e32 v109, v115, v107
	v_max_f32_e32 v108, 0, v108
	v_max_f32_e32 v109, 0, v109
	v_cvt_pk_f16_f32 v55, v108, v109
	ds_write_b64 v36, v[54:55] offset:8
	v_lshlrev_b32_e32 v124, 16, v92
	v_and_b32_e32 v125, 0xffff0000, v92
	v_lshlrev_b32_e32 v126, 16, v76
	v_and_b32_e32 v127, 0xffff0000, v76
	v_add_f32_e32 v124, v126, v124
	v_add_f32_e32 v125, v127, v125
	v_fma_f32 v126, v116, v51, v120
	v_fma_f32 v127, v117, v51, v121
	v_fmac_f32_e32 v126, v112, v124
	v_fmac_f32_e32 v127, v113, v125
	v_max_f32_e32 v126, 0, v126
	v_max_f32_e32 v127, 0, v127
	v_cvt_pk_f16_f32 v56, v126, v127
	v_lshlrev_b32_e32 v106, 16, v93
	v_and_b32_e32 v107, 0xffff0000, v93
	v_lshlrev_b32_e32 v108, 16, v77
	v_and_b32_e32 v109, 0xffff0000, v77
	v_add_f32_e32 v106, v108, v106
	v_add_f32_e32 v107, v109, v107
	v_fma_f32 v108, v118, v51, v122
	v_fma_f32 v109, v119, v51, v123
	v_fmac_f32_e32 v108, v114, v106
	v_fmac_f32_e32 v109, v115, v107
	v_max_f32_e32 v108, 0, v108
	v_max_f32_e32 v109, 0, v109
	v_cvt_pk_f16_f32 v57, v108, v109
	ds_write_b64 v36, v[56:57] offset:136
	v_lshlrev_b32_e32 v124, 16, v96
	v_and_b32_e32 v125, 0xffff0000, v96
	v_lshlrev_b32_e32 v126, 16, v80
	v_and_b32_e32 v127, 0xffff0000, v80
	v_add_f32_e32 v124, v126, v124
	v_add_f32_e32 v125, v127, v125
	v_fma_f32 v126, v116, v52, v120
	v_fma_f32 v127, v117, v52, v121
	v_fmac_f32_e32 v126, v112, v124
	v_fmac_f32_e32 v127, v113, v125
	v_max_f32_e32 v126, 0, v126
	v_max_f32_e32 v127, 0, v127
	v_cvt_pk_f16_f32 v54, v126, v127
	v_lshlrev_b32_e32 v106, 16, v97
	v_and_b32_e32 v107, 0xffff0000, v97
	v_lshlrev_b32_e32 v108, 16, v81
	v_and_b32_e32 v109, 0xffff0000, v81
	v_add_f32_e32 v106, v108, v106
	v_add_f32_e32 v107, v109, v107
	v_fma_f32 v108, v118, v52, v122
	v_fma_f32 v109, v119, v52, v123
	v_fmac_f32_e32 v108, v114, v106
	v_fmac_f32_e32 v109, v115, v107
	v_max_f32_e32 v108, 0, v108
	v_max_f32_e32 v109, 0, v109
	v_cvt_pk_f16_f32 v55, v108, v109
	ds_write_b64 v37, v[54:55] offset:264
	v_lshlrev_b32_e32 v124, 16, v104
	v_and_b32_e32 v125, 0xffff0000, v104
	v_lshlrev_b32_e32 v126, 16, v84
	v_and_b32_e32 v127, 0xffff0000, v84
	v_add_f32_e32 v124, v126, v124
	v_add_f32_e32 v125, v127, v125
	v_fma_f32 v126, v116, v53, v120
	v_fma_f32 v127, v117, v53, v121
	v_fmac_f32_e32 v126, v112, v124
	v_fmac_f32_e32 v127, v113, v125
	v_max_f32_e32 v126, 0, v126
	v_max_f32_e32 v127, 0, v127
	v_cvt_pk_f16_f32 v56, v126, v127
	v_lshlrev_b32_e32 v106, 16, v105
	v_and_b32_e32 v107, 0xffff0000, v105
	v_lshlrev_b32_e32 v108, 16, v85
	v_and_b32_e32 v109, 0xffff0000, v85
	v_add_f32_e32 v106, v108, v106
	v_add_f32_e32 v107, v109, v107
	v_fma_f32 v108, v118, v53, v122
	v_fma_f32 v109, v119, v53, v123
	v_fmac_f32_e32 v108, v114, v106
	v_fmac_f32_e32 v109, v115, v107
	v_max_f32_e32 v108, 0, v108
	v_max_f32_e32 v109, 0, v109
	v_cvt_pk_f16_f32 v57, v108, v109
	ds_write_b64 v37, v[56:57] offset:392
	s_waitcnt vmcnt(0)
	s_cmp_eq_u32 s15, 1
	s_cbranch_scc1 .Lcu_skip1
	v_min_u32_e32 v42, s35, v42
	v_min_u32_e32 v46, s35, v46
	v_min_u32_e32 v43, s35, v43
	v_min_u32_e32 v47, s35, v47
	v_min_u32_e32 v44, s35, v44
	v_min_u32_e32 v48, s35, v48
	v_min_u32_e32 v45, s35, v45
	v_min_u32_e32 v49, s35, v49
	v_lshl_or_b32 v42, v42, 7, v34
	v_lshl_or_b32 v46, v46, 7, v34
	v_lshl_or_b32 v43, v43, 7, v34
	v_lshl_or_b32 v47, v47, 7, v34
	v_lshl_or_b32 v44, v44, 7, v34
	v_lshl_or_b32 v48, v48, 7, v34
	v_lshl_or_b32 v45, v45, 7, v34
	v_lshl_or_b32 v49, v49, 7, v34
	global_load_dwordx4 v[70:73], v42, s[24:25]
	global_load_dwordx4 v[74:77], v43, s[24:25]
	global_load_dwordx4 v[78:81], v44, s[24:25]
	global_load_dwordx4 v[82:85], v45, s[24:25]
	s_lshl_b32 s34, s20, 2
	s_add_i32 s34, s34, 0x80
	v_add_u32_e32 v39, s34, v35
	global_load_dwordx4 v[50:53], v39, s[8:9]
.Lcu_skip1:
	v_subrev_u32_e32 v101, s20, v40
	v_subrev_u32_e32 v110, s20, v41
	v_med3_i32 v101, v101, 0, 32
	v_med3_i32 v110, v110, 0, 32
	v_lshlrev_b64 v[54:55], v101, 1
	v_lshlrev_b64 v[56:57], v110, 1
	v_add_u32_e32 v54, -1, v54
	v_add_u32_e32 v56, -1, v56
	v_xor_b32_e32 v101, v54, v56
	v_lshrrev_b32_e32 v110, 3, v100
	v_lshrrev_b32_e32 v101, v110, v101
	v_xor_b32_e32 v110, 16, v38
	v_xor_b32_e32 v111, 32, v38
	v_xor_b32_e32 v39, 48, v38
	s_waitcnt lgkmcnt(0)
	ds_read_b128 v[86:89], v38
	ds_read_b128 v[90:93], v110
	ds_read_b128 v[94:97], v111
	ds_read_b128 v[102:105], v39
	ds_read_b128 v[62:65], v99
	ds_read_b128 v[42:45], v99 offset:1024
	v_bfe_u32 v54, v101, 0, 2
	v_lshl_or_b32 v54, v54, 15, v54
	v_and_b32_e32 v54, 0x10001, v54
	v_mul_u32_u24_e32 v54, 0x3f80, v54
	v_bfe_u32 v55, v101, 2, 2
	v_lshl_or_b32 v55, v55, 15, v55
	v_and_b32_e32 v55, 0x10001, v55
	v_mul_u32_u24_e32 v55, 0x3f80, v55
	v_bfe_u32 v56, v101, 8, 2
	v_lshl_or_b32 v56, v56, 15, v56
	v_and_b32_e32 v56, 0x10001, v56
	v_mul_u32_u24_e32 v56, 0x3f80, v56
	v_bfe_u32 v57, v101, 10, 2
	v_lshl_or_b32 v57, v57, 15, v57
	v_and_b32_e32 v57, 0x10001, v57
	v_mul_u32_u24_e32 v57, 0x3f80, v57
	v_bfe_u32 v58, v101, 16, 2
	v_lshl_or_b32 v58, v58, 15, v58
	v_and_b32_e32 v58, 0x10001, v58
	v_mul_u32_u24_e32 v58, 0x3f80, v58
	v_bfe_u32 v59, v101, 18, 2
	v_lshl_or_b32 v59, v59, 15, v59
	v_and_b32_e32 v59, 0x10001, v59
	v_mul_u32_u24_e32 v59, 0x3f80, v59
	v_bfe_u32 v60, v101, 24, 2
	v_lshl_or_b32 v60, v60, 15, v60
	v_and_b32_e32 v60, 0x10001, v60
	v_mul_u32_u24_e32 v60, 0x3f80, v60
	v_bfe_u32 v61, v101, 26, 2
	v_lshl_or_b32 v61, v61, 15, v61
	v_and_b32_e32 v61, 0x10001, v61
	v_mul_u32_u24_e32 v61, 0x3f80, v61
	s_waitcnt lgkmcnt(1)
	v_mfma_f32_32x32x16_f16 v[112:127], v[86:89], v[62:65], 0
	ds_read_b128 v[62:65], v99 offset:2048
	s_waitcnt lgkmcnt(1)
	v_mfma_f32_32x32x16_f16 v[112:127], v[90:93], v[42:45], v[112:127]
	ds_read_b128 v[42:45], v99 offset:3072
	s_waitcnt lgkmcnt(1)
	v_mfma_f32_32x32x16_f16 v[112:127], v[94:97], v[62:65], v[112:127]
	ds_read_b128 v[62:65], v99 offset:4096
	s_waitcnt lgkmcnt(1)
	v_mfma_f32_32x32x16_f16 v[112:127], v[102:105], v[42:45], v[112:127]
	ds_read_b128 v[42:45], v99 offset:5120
	s_nop 11
	v_fma_f32 v110, v66, v112, v68
	v_fma_f32 v111, v66, v113, v68
	v_max_f32_e32 v110, 0, v110
	v_max_f32_e32 v111, 0, v111
	v_cvt_pk_bf16_f32 v106, v110, v111
	v_fma_f32 v110, v66, v114, v68
	v_fma_f32 v111, v66, v115, v68
	v_max_f32_e32 v110, 0, v110
	v_max_f32_e32 v111, 0, v111
	v_cvt_pk_bf16_f32 v107, v110, v111
	v_fma_f32 v110, v66, v116, v68
	v_fma_f32 v111, v66, v117, v68
	v_max_f32_e32 v110, 0, v110
	v_max_f32_e32 v111, 0, v111
	v_cvt_pk_bf16_f32 v108, v110, v111
	v_fma_f32 v110, v66, v118, v68
	v_fma_f32 v111, v66, v119, v68
	v_max_f32_e32 v110, 0, v110
	v_max_f32_e32 v111, 0, v111
	v_cvt_pk_bf16_f32 v109, v110, v111
	s_nop 1
	v_mfma_f32_32x32x16_bf16 v[18:33], v[106:109], v[54:57], v[18:33]
	v_fma_f32 v110, v66, v120, v68
	v_fma_f32 v111, v66, v121, v68
	v_max_f32_e32 v110, 0, v110
	v_max_f32_e32 v111, 0, v111
	v_cvt_pk_bf16_f32 v106, v110, v111
	v_fma_f32 v110, v66, v122, v68
	v_fma_f32 v111, v66, v123, v68
	v_max_f32_e32 v110, 0, v110
	v_max_f32_e32 v111, 0, v111
	v_cvt_pk_bf16_f32 v107, v110, v111
	v_fma_f32 v110, v66, v124, v68
	v_fma_f32 v111, v66, v125, v68
	v_max_f32_e32 v110, 0, v110
	v_max_f32_e32 v111, 0, v111
	v_cvt_pk_bf16_f32 v108, v110, v111
	v_fma_f32 v110, v66, v126, v68
	v_fma_f32 v111, v66, v127, v68
	v_max_f32_e32 v110, 0, v110
	v_max_f32_e32 v111, 0, v111
	v_cvt_pk_bf16_f32 v109, v110, v111
	s_nop 1
	v_mfma_f32_32x32x16_bf16 v[18:33], v[106:109], v[58:61], v[18:33]
	s_waitcnt lgkmcnt(1)
	v_mfma_f32_32x32x16_f16 v[112:127], v[86:89], v[62:65], 0
	ds_read_b128 v[62:65], v99 offset:6144
	s_waitcnt lgkmcnt(1)
	v_mfma_f32_32x32x16_f16 v[112:127], v[90:93], v[42:45], v[112:127]
	ds_read_b128 v[42:45], v99 offset:7168
	s_waitcnt lgkmcnt(1)
	v_mfma_f32_32x32x16_f16 v[112:127], v[94:97], v[62:65], v[112:127]
	s_waitcnt lgkmcnt(0)
	v_mfma_f32_32x32x16_f16 v[112:127], v[102:105], v[42:45], v[112:127]
	s_cmp_eq_u32 s15, 1
	s_cbranch_scc1 .Lcu_skip2
	global_load_dwordx4 v[86:89], v46, s[10:11]
	global_load_dwordx4 v[90:93], v47, s[10:11]
	global_load_dwordx4 v[94:97], v48, s[10:11]
	global_load_dwordx4 v[102:105], v49, s[10:11]
	s_add_i32 s34, s34, 0x80
	v_add_u32_e32 v39, s34, v35
	global_load_dwordx4 v[42:45], v39, s[4:5]
	global_load_dwordx4 v[46:49], v39, s[6:7]
.Lcu_skip2:
	s_nop 9
	v_fma_f32 v110, v67, v112, v69
	v_fma_f32 v111, v67, v113, v69
	v_max_f32_e32 v110, 0, v110
	v_max_f32_e32 v111, 0, v111
	v_cvt_pk_bf16_f32 v106, v110, v111
	v_fma_f32 v110, v67, v114, v69
	v_fma_f32 v111, v67, v115, v69
	v_max_f32_e32 v110, 0, v110
	v_max_f32_e32 v111, 0, v111
	v_cvt_pk_bf16_f32 v107, v110, v111
	v_fma_f32 v110, v67, v116, v69
	v_fma_f32 v111, v67, v117, v69
	v_max_f32_e32 v110, 0, v110
	v_max_f32_e32 v111, 0, v111
	v_cvt_pk_bf16_f32 v108, v110, v111
	v_fma_f32 v110, v67, v118, v69
	v_fma_f32 v111, v67, v119, v69
	v_max_f32_e32 v110, 0, v110
	v_max_f32_e32 v111, 0, v111
	v_cvt_pk_bf16_f32 v109, v110, v111
	s_nop 1
	v_mfma_f32_32x32x16_bf16 v[2:17], v[106:109], v[54:57], v[2:17]
	v_fma_f32 v110, v67, v120, v69
	v_fma_f32 v111, v67, v121, v69
	v_max_f32_e32 v110, 0, v110
	v_max_f32_e32 v111, 0, v111
	v_cvt_pk_bf16_f32 v106, v110, v111
	v_fma_f32 v110, v67, v122, v69
	v_fma_f32 v111, v67, v123, v69
	v_max_f32_e32 v110, 0, v110
	v_max_f32_e32 v111, 0, v111
	v_cvt_pk_bf16_f32 v107, v110, v111
	v_fma_f32 v110, v67, v124, v69
	v_fma_f32 v111, v67, v125, v69
	v_max_f32_e32 v110, 0, v110
	v_max_f32_e32 v111, 0, v111
	v_cvt_pk_bf16_f32 v108, v110, v111
	v_fma_f32 v110, v67, v126, v69
	v_fma_f32 v111, v67, v127, v69
	v_max_f32_e32 v110, 0, v110
	v_max_f32_e32 v111, 0, v111
	v_cvt_pk_bf16_f32 v109, v110, v111
	s_nop 1
	v_mfma_f32_32x32x16_bf16 v[2:17], v[106:109], v[58:61], v[2:17]
	s_add_i32 s20, s20, 32
	s_add_i32 s15, s15, -1
	s_cmp_lg_u32 s15, 0
	s_cbranch_scc1 .Lcu_loop
	v_or_b32_e32 v90, s14, v98
	s_branch .LBB8_8

	.amdhsa_kernel _Z8k_passCUILi1EEvPKiS1_PKfPKtS5_S3_S3_S3_S3_S3_S3_PK15HIP_vector_typeIjLj4EES9_S9_PKdSB_S1_S1_S5_S3_PtPd
		.amdhsa_group_segment_fixed_size 79104
		.amdhsa_private_segment_fixed_size 0
		.amdhsa_kernarg_size 432
		.amdhsa_user_sgpr_count 2
		.amdhsa_user_sgpr_dispatch_ptr 0
		.amdhsa_user_sgpr_queue_ptr 0
		.amdhsa_user_sgpr_kernarg_segment_ptr 1
		.amdhsa_user_sgpr_dispatch_id 0
		.amdhsa_user_sgpr_kernarg_preload_length 0
		.amdhsa_user_sgpr_kernarg_preload_offset 0
		.amdhsa_user_sgpr_private_segment_size 0
		.amdhsa_uses_dynamic_stack 0
		.amdhsa_enable_private_segment 0
		.amdhsa_system_sgpr_workgroup_id_x 1
		.amdhsa_system_sgpr_workgroup_id_y 0
		.amdhsa_system_sgpr_workgroup_id_z 0
		.amdhsa_system_sgpr_workgroup_info 0
		.amdhsa_system_vgpr_workitem_id 0
		.amdhsa_next_free_vgpr 128
		.amdhsa_next_free_sgpr 91
		.amdhsa_accum_offset 128
		.amdhsa_reserve_vcc 1
		.amdhsa_float_round_mode_32 0
		.amdhsa_float_round_mode_16_64 0
		.amdhsa_float_denorm_mode_32 3
		.amdhsa_float_denorm_mode_16_64 3
		.amdhsa_dx10_clamp 1
		.amdhsa_ieee_mode 1
		.amdhsa_fp16_overflow 0
		.amdhsa_tg_split 0
		.amdhsa_exception_fp_ieee_invalid_op 0
		.amdhsa_exception_fp_denorm_src 0
		.amdhsa_exception_fp_ieee_div_zero 0
		.amdhsa_exception_fp_ieee_overflow 0
		.amdhsa_exception_fp_ieee_underflow 0
		.amdhsa_exception_fp_ieee_inexact 0
		.amdhsa_exception_int_div_zero 0
	.end_amdhsa_kernel

_Z4k_U3ILb0EtEvPKtPtPKdPKfS6_PK15HIP_vector_typeIjLj4EES6_PT0_SC_S6_Pd:
	s_load_dwordx2 s[4:5], s[0:1], 0x28
	s_load_dwordx4 s[20:23], s[0:1], 0x0
	s_load_dword s24, s[0:1], 0x58
	v_mov_b32_e32 v3, 0
	v_lshlrev_b32_e32 v2, 4, v0
	v_or_b32_e32 v1, 0x4000, v2
	s_movk_i32 s3, 0x1000
	s_waitcnt lgkmcnt(0)
	v_lshrrev_b32_e32 v78, 6, v0
	v_mul_lo_u32 v78, s24, v78
	v_add_u32_e32 v78, s2, v78
	v_min_u32_e32 v78, 0xc34, v78
	v_and_b32_e32 v79, 31, v0
	v_lshl_or_b32 v78, v78, 5, v79
	v_and_b32_e32 v79, 32, v0
	v_lshlrev_b32_e32 v78, 7, v78
	v_lshl_add_u32 v78, v79, 1, v78
	global_load_dwordx4 v[44:47], v78, s[22:23] offset:48
	global_load_dwordx4 v[48:51], v78, s[22:23] offset:32
	global_load_dwordx4 v[52:55], v78, s[22:23] offset:16
	global_load_dwordx4 v[56:59], v78, s[22:23]
	global_load_dwordx4 v[60:63], v78, s[20:21] offset:48
	global_load_dwordx4 v[64:67], v78, s[20:21] offset:32
	global_load_dwordx4 v[68:71], v78, s[20:21] offset:16
	global_load_dwordx4 v[72:75], v78, s[20:21]
	v_lshl_add_u64 v[32:33], s[4:5], 0, v[2:3]
	v_add_co_u32_e32 v24, vcc, 0x1000, v32
	global_load_dwordx4 v[4:7], v2, s[4:5]
	s_nop 0
	v_addc_co_u32_e32 v25, vcc, 0, v33, vcc
	v_add_co_u32_e32 v26, vcc, 0x2000, v32
	s_nop 1
	v_addc_co_u32_e32 v27, vcc, 0, v33, vcc
	v_add_co_u32_e32 v28, vcc, 0x3000, v32
	s_nop 1
	v_addc_co_u32_e32 v29, vcc, 0, v33, vcc
	v_add_co_u32_e32 v34, vcc, 0x5000, v32
	global_load_dwordx4 v[8:11], v[26:27], off
	global_load_dwordx4 v[12:15], v[28:29], off
	global_load_dwordx4 v[16:19], v[24:25], off
	global_load_dwordx4 v[20:23], v1, s[4:5]
	v_addc_co_u32_e32 v35, vcc, 0, v33, vcc
	v_add_co_u32_e32 v36, vcc, 0x6000, v32
	s_nop 1
	v_addc_co_u32_e32 v37, vcc, 0, v33, vcc
	global_load_dwordx4 v[24:27], v[34:35], off
	global_load_dwordx4 v[28:31], v[36:37], off
	v_add_co_u32_e32 v32, vcc, 0x7000, v32
	s_nop 1
	v_addc_co_u32_e32 v33, vcc, 0, v33, vcc
	global_load_dwordx4 v[32:35], v[32:33], off
	v_cmp_gt_u32_e32 vcc, 64, v0
	s_waitcnt vmcnt(7)
	ds_write_b128 v2, v[4:7]
	s_waitcnt vmcnt(4)
	ds_write_b128 v2, v[16:19] offset:4096
	s_waitcnt vmcnt(3)
	ds_write_b128 v2, v[20:23] offset:16384
	ds_write_b128 v2, v[8:11] offset:8192
	ds_write_b128 v2, v[12:15] offset:12288
	s_waitcnt vmcnt(2)
	ds_write_b128 v2, v[24:27] offset:20480
	s_waitcnt vmcnt(1)
	ds_write_b128 v2, v[28:31] offset:24576
	s_waitcnt vmcnt(0)
	ds_write_b128 v2, v[32:35] offset:28672
	v_lshlrev_b32_e32 v10, 2, v0
	s_and_saveexec_b64 s[6:7], vcc
	s_cbranch_execz .LBB9_2
	s_load_dwordx4 s[8:11], s[0:1], 0x10
	s_load_dwordx2 s[4:5], s[0:1], 0x20
	v_lshlrev_b32_e32 v2, 3, v0
	s_mov_b32 s12, 0
	s_brev_b32 s13, 8
	s_waitcnt lgkmcnt(0)
	global_load_dwordx2 v[6:7], v2, s[8:9]
	global_load_dwordx2 v[8:9], v2, s[8:9] offset:512
	global_load_dwordx2 v[12:13], v2, s[8:9] offset:1024
	global_load_dwordx2 v[14:15], v2, s[8:9] offset:1536
	global_load_dwordx2 v[16:17], v2, s[8:9] offset:2048
	global_load_dwordx2 v[18:19], v2, s[8:9] offset:2560
	global_load_dwordx2 v[20:21], v2, s[8:9] offset:3072
	global_load_dwordx2 v[22:23], v2, s[8:9] offset:3584
	v_lshl_add_u64 v[4:5], s[8:9], 0, v[2:3]
	v_add_co_u32_e32 v2, vcc, s3, v4
	s_mov_b32 s8, 0x88e368f1
	s_nop 0
	v_addc_co_u32_e32 v3, vcc, 0, v5, vcc
	global_load_dwordx2 v[4:5], v[2:3], off
	global_load_dwordx2 v[24:25], v[2:3], off offset:512
	global_load_dwordx2 v[26:27], v[2:3], off offset:1024
	global_load_dwordx2 v[28:29], v[2:3], off offset:1536
	global_load_dwordx2 v[30:31], v[2:3], off offset:2048
	global_load_dwordx2 v[32:33], v[2:3], off offset:2560
	global_load_dwordx2 v[34:35], v[2:3], off offset:3072
	global_load_dwordx2 v[36:37], v[2:3], off offset:3584
	global_load_dword v1, v10, s[10:11]
	global_load_dword v11, v10, s[4:5]
	s_mov_b32 s10, 0
	s_mov_b32 s11, 0x40f86a00
	s_mov_b32 s9, 0x3ee4f8b5
	v_mov_b32_e32 v38, 0x100
	v_mov_b32_e32 v39, 0xffffff80
	v_mov_b32_e32 v40, 0x260
	s_waitcnt vmcnt(17)
	v_add_f64 v[2:3], v[6:7], 0
	s_waitcnt vmcnt(16)
	v_add_f64 v[6:7], v[8:9], 0
	s_waitcnt vmcnt(15)
	v_add_f64 v[2:3], v[2:3], v[12:13]
	s_waitcnt vmcnt(14)
	v_add_f64 v[6:7], v[6:7], v[14:15]
	s_waitcnt vmcnt(13)
	v_add_f64 v[2:3], v[2:3], v[16:17]
	s_waitcnt vmcnt(12)
	v_add_f64 v[6:7], v[6:7], v[18:19]
	s_waitcnt vmcnt(11)
	v_add_f64 v[2:3], v[2:3], v[20:21]
	s_waitcnt vmcnt(10)
	v_add_f64 v[6:7], v[6:7], v[22:23]
	s_waitcnt vmcnt(9)
	v_add_f64 v[2:3], v[2:3], v[4:5]
	s_waitcnt vmcnt(8)
	v_add_f64 v[4:5], v[6:7], v[24:25]
	s_waitcnt vmcnt(7)
	v_add_f64 v[2:3], v[2:3], v[26:27]
	s_waitcnt vmcnt(6)
	v_add_f64 v[4:5], v[4:5], v[28:29]
	s_waitcnt vmcnt(5)
	v_add_f64 v[2:3], v[2:3], v[30:31]
	s_waitcnt vmcnt(4)
	v_add_f64 v[4:5], v[4:5], v[32:33]
	s_waitcnt vmcnt(3)
	v_add_f64 v[2:3], v[2:3], v[34:35]
	s_waitcnt vmcnt(2)
	v_add_f64 v[4:5], v[4:5], v[36:37]
	v_div_scale_f64 v[6:7], s[4:5], s[10:11], s[10:11], v[2:3]
	v_div_scale_f64 v[12:13], s[4:5], s[10:11], s[10:11], v[4:5]
	v_rcp_f64_e32 v[14:15], v[6:7]
	v_rcp_f64_e32 v[16:17], v[12:13]
	v_div_scale_f64 v[8:9], vcc, v[2:3], s[10:11], v[2:3]
	v_fma_f64 v[20:21], -v[6:7], v[14:15], 1.0
	v_fma_f64 v[22:23], -v[12:13], v[16:17], 1.0
	v_fmac_f64_e32 v[14:15], v[14:15], v[20:21]
	v_fmac_f64_e32 v[16:17], v[16:17], v[22:23]
	v_fma_f64 v[20:21], -v[6:7], v[14:15], 1.0
	v_fma_f64 v[22:23], -v[12:13], v[16:17], 1.0
	v_fmac_f64_e32 v[14:15], v[14:15], v[20:21]
	v_div_scale_f64 v[18:19], s[4:5], v[4:5], s[10:11], v[4:5]
	v_fmac_f64_e32 v[16:17], v[16:17], v[22:23]
	v_mul_f64 v[20:21], v[8:9], v[14:15]
	v_mul_f64 v[22:23], v[18:19], v[16:17]
	v_fma_f64 v[6:7], -v[6:7], v[20:21], v[8:9]
	v_fma_f64 v[8:9], -v[12:13], v[22:23], v[18:19]
	v_div_fmas_f64 v[6:7], v[6:7], v[14:15], v[20:21]
	s_mov_b64 vcc, s[4:5]
	v_div_fixup_f64 v[2:3], v[6:7], s[10:11], v[2:3]
	v_div_fmas_f64 v[6:7], v[8:9], v[16:17], v[22:23]
	v_div_fixup_f64 v[4:5], v[6:7], s[10:11], v[4:5]
	v_fma_f64 v[4:5], -v[2:3], v[2:3], v[4:5]
	v_cmp_ngt_f64_e32 vcc, 0, v[4:5]
	s_waitcnt vmcnt(1)
	v_cvt_f64_f32_e32 v[8:9], v1
	s_waitcnt vmcnt(0)
	v_cvt_f64_f32_e32 v[12:13], v11
	v_cndmask_b32_e32 v5, 0, v5, vcc
	v_cndmask_b32_e32 v4, 0, v4, vcc
	v_add_f64 v[4:5], v[4:5], s[8:9]
	v_cmp_gt_f64_e32 vcc, s[12:13], v[4:5]
	v_add_f64 v[2:3], v[2:3], 0
	s_nop 0
	v_cndmask_b32_e32 v6, 0, v38, vcc
	v_ldexp_f64 v[4:5], v[4:5], v6
	v_rsq_f64_e32 v[6:7], v[4:5]
	v_cndmask_b32_e32 v1, 0, v39, vcc
	v_cmp_class_f64_e32 vcc, v[4:5], v40
	v_mul_f64 v[14:15], v[4:5], v[6:7]
	v_mul_f64 v[6:7], v[6:7], 0.5
	v_fma_f64 v[16:17], -v[6:7], v[14:15], 0.5
	v_fmac_f64_e32 v[14:15], v[14:15], v[16:17]
	v_fmac_f64_e32 v[6:7], v[6:7], v[16:17]
	v_fma_f64 v[16:17], -v[14:15], v[14:15], v[4:5]
	v_fmac_f64_e32 v[14:15], v[16:17], v[6:7]
	v_fma_f64 v[16:17], -v[14:15], v[14:15], v[4:5]
	v_fmac_f64_e32 v[14:15], v[16:17], v[6:7]
	v_ldexp_f64 v[6:7], v[14:15], v1
	v_cndmask_b32_e32 v5, v7, v5, vcc
	v_cndmask_b32_e32 v4, v6, v4, vcc
	v_div_scale_f64 v[6:7], s[4:5], v[4:5], v[4:5], v[8:9]
	v_rcp_f64_e32 v[14:15], v[6:7]
	v_div_scale_f64 v[16:17], vcc, v[8:9], v[4:5], v[8:9]
	v_fma_f64 v[18:19], -v[6:7], v[14:15], 1.0
	v_fmac_f64_e32 v[14:15], v[14:15], v[18:19]
	v_fma_f64 v[18:19], -v[6:7], v[14:15], 1.0
	v_fmac_f64_e32 v[14:15], v[14:15], v[18:19]
	v_mul_f64 v[18:19], v[16:17], v[14:15]
	v_fma_f64 v[6:7], -v[6:7], v[18:19], v[16:17]
	v_div_fmas_f64 v[6:7], v[6:7], v[14:15], v[18:19]
	v_div_fixup_f64 v[4:5], v[6:7], v[4:5], v[8:9]
	v_fma_f64 v[2:3], -v[2:3], v[4:5], v[12:13]
	v_cvt_f32_f64_e32 v1, v[4:5]
	v_cvt_f32_f64_e32 v2, v[2:3]
	ds_write2st64_b32 v10, v1, v2 offset0:128 offset1:129
.LBB9_2:
	s_or_b64 exec, exec, s[6:7]
	s_waitcnt lgkmcnt(0)
	s_barrier
	s_load_dword s3, s[0:1], 0x58
	v_lshrrev_b32_e32 v1, 6, v0
	s_waitcnt lgkmcnt(0)
	v_mul_lo_u32 v1, s3, v1
	v_add_u32_e32 v1, s2, v1
	s_movk_i32 s2, 0xc35
	v_cmp_gt_i32_e32 vcc, s2, v1
	s_and_saveexec_b64 s[2:3], vcc
	s_cbranch_execz .LBB9_4
	s_load_dwordx4 s[4:7], s[0:1], 0x30
	s_load_dwordx2 s[2:3], s[0:1], 0x40
	s_load_dwordx4 s[8:11], s[0:1], 0x0
	v_and_b32_e32 v22, 31, v0
	v_lshlrev_b32_e32 v1, 5, v1
	v_or_b32_e32 v2, v1, v22
	v_ashrrev_i32_e32 v3, 31, v2
	v_lshlrev_b64 v[16:17], 7, v[2:3]
	v_and_b32_e32 v4, 32, v0
	s_waitcnt lgkmcnt(0)
	v_lshl_add_u64 v[2:3], s[10:11], 0, v[16:17]
	v_lshlrev_b32_e32 v28, 1, v4
	v_mov_b32_e32 v29, 0
	v_lshl_add_u64 v[18:19], v[2:3], 0, v[28:29]
	s_waitcnt vmcnt(0)
	v_mov_b32_e32 v2, v44
	v_mov_b32_e32 v3, v45
	v_mov_b32_e32 v4, v46
	v_mov_b32_e32 v5, v47
	v_mov_b32_e32 v6, v48
	v_mov_b32_e32 v7, v49
	v_mov_b32_e32 v8, v50
	v_mov_b32_e32 v9, v51
	v_mov_b32_e32 v12, v52
	v_mov_b32_e32 v13, v53
	v_mov_b32_e32 v14, v54
	v_mov_b32_e32 v15, v55
	v_mov_b32_e32 v24, v56
	v_mov_b32_e32 v25, v57
	v_mov_b32_e32 v26, v58
	v_mov_b32_e32 v27, v59
	v_lshl_add_u64 v[16:17], s[8:9], 0, v[16:17]
	v_lshl_add_u64 v[16:17], v[16:17], 0, v[28:29]
	v_and_b32_e32 v76, 0x80, v10
	v_and_b32_e32 v20, 63, v0
	v_lshrrev_b32_e32 v0, 3, v0
	v_and_or_b32 v0, v0, 4, v1
	v_ashrrev_i32_e32 v1, 31, v0
	s_waitcnt vmcnt(0)
	v_mov_b32_e32 v28, v60
	v_mov_b32_e32 v29, v61
	v_mov_b32_e32 v30, v62
	v_mov_b32_e32 v31, v63
	v_mov_b32_e32 v32, v64
	v_mov_b32_e32 v33, v65
	v_mov_b32_e32 v34, v66
	v_mov_b32_e32 v35, v67
	v_mov_b32_e32 v36, v68
	v_mov_b32_e32 v37, v69
	v_mov_b32_e32 v38, v70
	v_mov_b32_e32 v39, v71
	v_mov_b32_e32 v40, v72
	v_mov_b32_e32 v41, v73
	v_mov_b32_e32 v42, v74
	v_mov_b32_e32 v43, v75
	v_cvt_f32_f16_sdwa v17, v24 dst_sel:DWORD dst_unused:UNUSED_PAD src0_sel:WORD_1
	s_waitcnt vmcnt(0)
	v_lshlrev_b32_e32 v11, 16, v40
	v_and_b32_e32 v16, 0xffff0000, v40
	v_lshlrev_b32_e32 v21, 16, v41
	v_and_b32_e32 v23, 0xffff0000, v41
	v_lshlrev_b32_e32 v48, 16, v42
	v_and_b32_e32 v49, 0xffff0000, v42
	v_lshlrev_b32_e32 v50, 16, v43
	v_and_b32_e32 v51, 0xffff0000, v43
	v_lshlrev_b32_e32 v52, 16, v36
	v_and_b32_e32 v53, 0xffff0000, v36
	v_lshlrev_b32_e32 v54, 16, v37
	v_and_b32_e32 v55, 0xffff0000, v37
	v_lshlrev_b32_e32 v56, 16, v38
	v_and_b32_e32 v57, 0xffff0000, v38
	v_lshlrev_b32_e32 v58, 16, v39
	v_and_b32_e32 v59, 0xffff0000, v39
	v_lshlrev_b32_e32 v60, 16, v32
	v_and_b32_e32 v61, 0xffff0000, v32
	v_lshlrev_b32_e32 v62, 16, v33
	v_and_b32_e32 v63, 0xffff0000, v33
	v_lshlrev_b32_e32 v64, 16, v34
	v_and_b32_e32 v65, 0xffff0000, v34
	v_lshlrev_b32_e32 v66, 16, v35
	v_and_b32_e32 v67, 0xffff0000, v35
	v_lshlrev_b32_e32 v68, 16, v28
	v_and_b32_e32 v69, 0xffff0000, v28
	v_lshlrev_b32_e32 v70, 16, v29
	v_and_b32_e32 v71, 0xffff0000, v29
	v_lshlrev_b32_e32 v72, 16, v30
	v_and_b32_e32 v73, 0xffff0000, v30
	v_lshlrev_b32_e32 v74, 16, v31
	v_and_b32_e32 v75, 0xffff0000, v31
	ds_read_b128 v[28:31], v76 offset:32768
	ds_read_b128 v[32:35], v76 offset:32784
	ds_read_b128 v[36:39], v76 offset:32800
	ds_read_b128 v[40:43], v76 offset:32816
	ds_read_b128 v[44:47], v76 offset:33024
	s_waitcnt lgkmcnt(0)
	v_fma_f32 v10, v28, v11, v44
	v_fma_f32 v11, v29, v16, v45
	v_cvt_f32_f16_e32 v16, v24
	v_max_f32_e32 v10, 0, v10
	v_max_f32_e32 v11, 0, v11
	v_fmac_f32_e32 v47, v31, v23
	v_pk_add_f32 v[44:45], v[10:11], v[16:17]
	v_cvt_f32_f16_e32 v16, v25
	v_cvt_f32_f16_sdwa v17, v25 dst_sel:DWORD dst_unused:UNUSED_PAD src0_sel:WORD_1
	v_fma_f32 v10, v30, v21, v46
	ds_read_b128 v[28:31], v76 offset:33040
	v_max_f32_e32 v10, 0, v10
	v_max_f32_e32 v11, 0, v47
	v_pk_add_f32 v[46:47], v[10:11], v[16:17]
	v_cvt_f32_f16_e32 v16, v26
	v_cvt_f32_f16_sdwa v17, v26 dst_sel:DWORD dst_unused:UNUSED_PAD src0_sel:WORD_1
	s_waitcnt lgkmcnt(0)
	v_fma_f32 v10, v32, v48, v28
	v_fma_f32 v11, v33, v49, v29
	v_max_f32_e32 v10, 0, v10
	v_max_f32_e32 v11, 0, v11
	v_pk_add_f32 v[28:29], v[10:11], v[16:17]
	v_cvt_f32_f16_e32 v16, v27
	v_cvt_f32_f16_sdwa v17, v27 dst_sel:DWORD dst_unused:UNUSED_PAD src0_sel:WORD_1
	ds_read_b128 v[24:27], v76 offset:33056
	v_fma_f32 v10, v34, v50, v30
	v_fmac_f32_e32 v31, v35, v51
	v_max_f32_e32 v10, 0, v10
	v_max_f32_e32 v11, 0, v31
	v_pk_add_f32 v[30:31], v[10:11], v[16:17]
	v_cvt_f32_f16_e32 v16, v12
	v_cvt_f32_f16_sdwa v17, v12 dst_sel:DWORD dst_unused:UNUSED_PAD src0_sel:WORD_1
	s_waitcnt lgkmcnt(0)
	v_fma_f32 v10, v36, v52, v24
	v_fma_f32 v11, v37, v53, v25
	v_cvt_f32_f16_e32 v12, v13
	v_cvt_f32_f16_sdwa v13, v13 dst_sel:DWORD dst_unused:UNUSED_PAD src0_sel:WORD_1
	v_max_f32_e32 v10, 0, v10
	v_max_f32_e32 v11, 0, v11
	v_pk_add_f32 v[24:25], v[10:11], v[16:17]
	v_fma_f32 v10, v38, v54, v26
	v_fmac_f32_e32 v27, v39, v55
	v_max_f32_e32 v10, 0, v10
	v_max_f32_e32 v11, 0, v27
	v_pk_add_f32 v[26:27], v[10:11], v[12:13]
	ds_read_b128 v[10:13], v76 offset:33072
	v_cvt_f32_f16_e32 v16, v14
	v_cvt_f32_f16_sdwa v17, v14 dst_sel:DWORD dst_unused:UNUSED_PAD src0_sel:WORD_1
	v_lshlrev_b32_e32 v23, 4, v20
	s_waitcnt lgkmcnt(0)
	v_fma_f32 v10, v40, v56, v10
	v_fma_f32 v11, v41, v57, v11
	v_max_f32_e32 v10, 0, v10
	v_max_f32_e32 v11, 0, v11
	v_fmac_f32_e32 v13, v43, v59
	v_pk_add_f32 v[32:33], v[10:11], v[16:17]
	v_fma_f32 v10, v42, v58, v12
	v_max_f32_e32 v11, 0, v13
	v_cvt_f32_f16_e32 v12, v15
	v_cvt_f32_f16_sdwa v13, v15 dst_sel:DWORD dst_unused:UNUSED_PAD src0_sel:WORD_1
	v_max_f32_e32 v10, 0, v10
	v_pk_add_f32 v[34:35], v[10:11], v[12:13]
	ds_read_b128 v[10:13], v76 offset:32832
	ds_read_b128 v[14:17], v76 offset:33088
	s_waitcnt lgkmcnt(0)
	v_fma_f32 v10, v10, v60, v14
	v_fma_f32 v11, v11, v61, v15
	v_cvt_f32_f16_e32 v14, v6
	v_cvt_f32_f16_sdwa v15, v6 dst_sel:DWORD dst_unused:UNUSED_PAD src0_sel:WORD_1
	v_max_f32_e32 v10, 0, v10
	v_max_f32_e32 v11, 0, v11
	v_fma_f32 v6, v12, v62, v16
	v_pk_add_f32 v[36:37], v[10:11], v[14:15]
	v_max_f32_e32 v10, 0, v6
	v_cvt_f32_f16_e32 v6, v7
	v_cvt_f32_f16_sdwa v7, v7 dst_sel:DWORD dst_unused:UNUSED_PAD src0_sel:WORD_1
	v_fmac_f32_e32 v17, v13, v63
	v_max_f32_e32 v11, 0, v17
	v_pk_add_f32 v[38:39], v[10:11], v[6:7]
	ds_read_b128 v[10:13], v76 offset:32848
	ds_read_b128 v[14:17], v76 offset:33104
	s_waitcnt lgkmcnt(0)
	v_fma_f32 v6, v10, v64, v14
	v_fma_f32 v7, v11, v65, v15
	v_cvt_f32_f16_e32 v10, v8
	v_cvt_f32_f16_sdwa v11, v8 dst_sel:DWORD dst_unused:UNUSED_PAD src0_sel:WORD_1
	v_cvt_f32_f16_e32 v8, v9
	v_cvt_f32_f16_sdwa v9, v9 dst_sel:DWORD dst_unused:UNUSED_PAD src0_sel:WORD_1
	v_max_f32_e32 v6, 0, v6
	v_max_f32_e32 v7, 0, v7
	v_pk_add_f32 v[40:41], v[6:7], v[10:11]
	v_fma_f32 v6, v12, v66, v16
	v_fmac_f32_e32 v17, v13, v67
	v_max_f32_e32 v6, 0, v6
	v_max_f32_e32 v7, 0, v17
	v_pk_add_f32 v[42:43], v[6:7], v[8:9]
	ds_read_b128 v[6:9], v76 offset:32864
	ds_read_b128 v[10:13], v76 offset:33120
	v_cvt_pk_f16_f32 v14, v44, v45
	v_cvt_pk_f16_f32 v15, v46, v47
	v_cvt_pk_f16_f32 v16, v28, v29
	v_cvt_pk_f16_f32 v17, v30, v31
	s_waitcnt lgkmcnt(0)
	v_fma_f32 v6, v6, v68, v10
	v_fma_f32 v7, v7, v69, v11
	v_cvt_f32_f16_e32 v10, v2
	v_cvt_f32_f16_sdwa v11, v2 dst_sel:DWORD dst_unused:UNUSED_PAD src0_sel:WORD_1
	v_max_f32_e32 v6, 0, v6
	v_max_f32_e32 v7, 0, v7
	v_fma_f32 v2, v8, v70, v12
	v_pk_add_f32 v[48:49], v[6:7], v[10:11]
	v_max_f32_e32 v6, 0, v2
	v_cvt_f32_f16_e32 v2, v3
	v_cvt_f32_f16_sdwa v3, v3 dst_sel:DWORD dst_unused:UNUSED_PAD src0_sel:WORD_1
	v_fmac_f32_e32 v13, v9, v71
	v_max_f32_e32 v7, 0, v13
	v_pk_add_f32 v[50:51], v[6:7], v[2:3]
	ds_read_b128 v[6:9], v76 offset:32880
	ds_read_b128 v[10:13], v76 offset:33136
	global_store_dwordx4 v[18:19], v[14:17], off
	s_waitcnt lgkmcnt(0)
	v_fma_f32 v2, v6, v72, v10
	v_fma_f32 v3, v7, v73, v11
	v_cvt_f32_f16_e32 v6, v4
	v_cvt_f32_f16_sdwa v7, v4 dst_sel:DWORD dst_unused:UNUSED_PAD src0_sel:WORD_1
	v_cvt_f32_f16_e32 v4, v5
	v_cvt_f32_f16_sdwa v5, v5 dst_sel:DWORD dst_unused:UNUSED_PAD src0_sel:WORD_1
	v_max_f32_e32 v2, 0, v2
	v_max_f32_e32 v3, 0, v3
	v_pk_add_f32 v[52:53], v[2:3], v[6:7]
	v_fma_f32 v2, v8, v74, v12
	v_fmac_f32_e32 v13, v9, v75
	v_max_f32_e32 v2, 0, v2
	v_max_f32_e32 v3, 0, v13
	v_pk_add_f32 v[54:55], v[2:3], v[4:5]
	v_cvt_pk_f16_f32 v10, v24, v25
	v_cvt_pk_f16_f32 v11, v26, v27
	v_cvt_pk_f16_f32 v12, v32, v33
	v_cvt_pk_f16_f32 v13, v34, v35
	v_cvt_pk_f16_f32 v6, v36, v37
	v_cvt_pk_f16_f32 v7, v38, v39
	v_cvt_pk_f16_f32 v8, v40, v41
	v_cvt_pk_f16_f32 v9, v42, v43
	v_cvt_pk_f16_f32 v2, v48, v49
	v_cvt_pk_f16_f32 v3, v50, v51
	v_cvt_pk_f16_f32 v4, v52, v53
	v_cvt_pk_f16_f32 v5, v54, v55
	global_store_dwordx4 v[18:19], v[10:13], off offset:16
	global_store_dwordx4 v[18:19], v[6:9], off offset:32
	global_store_dwordx4 v[18:19], v[2:5], off offset:48
	v_lshlrev_b32_e32 v18, 3, v22
	global_load_dwordx2 a[0:1], v18, s[4:5]
	ds_read_b128 v[18:21], v23
	ds_read_b128 v[24:27], v23 offset:8192
	ds_read_b128 v[28:31], v23 offset:4096
	ds_read_b128 v[32:35], v23 offset:12288
	s_waitcnt vmcnt(0)
	v_accvgpr_mov_b32 a16, a0
	v_accvgpr_mov_b32 a17, a0
	v_accvgpr_mov_b32 a18, a0
	v_accvgpr_mov_b32 a19, a0
	v_accvgpr_mov_b32 a20, a0
	v_accvgpr_mov_b32 a21, a0
	v_accvgpr_mov_b32 a22, a0
	v_accvgpr_mov_b32 a23, a0
	v_accvgpr_mov_b32 a24, a0
	v_accvgpr_mov_b32 a25, a0
	v_accvgpr_mov_b32 a26, a0
	v_accvgpr_mov_b32 a27, a0
	v_accvgpr_mov_b32 a28, a0
	v_accvgpr_mov_b32 a29, a0
	v_accvgpr_mov_b32 a30, a0
	v_accvgpr_mov_b32 a31, a0
	v_accvgpr_mov_b32 a0, a1
	v_accvgpr_mov_b32 a2, a1
	v_accvgpr_mov_b32 a3, a1
	v_accvgpr_mov_b32 a4, a1
	v_accvgpr_mov_b32 a5, a1
	v_accvgpr_mov_b32 a6, a1
	v_accvgpr_mov_b32 a7, a1
	v_accvgpr_mov_b32 a8, a1
	v_accvgpr_mov_b32 a9, a1
	v_accvgpr_mov_b32 a10, a1
	v_accvgpr_mov_b32 a11, a1
	v_accvgpr_mov_b32 a12, a1
	v_accvgpr_mov_b32 a13, a1
	v_accvgpr_mov_b32 a14, a1
	v_accvgpr_mov_b32 a15, a1
	s_waitcnt lgkmcnt(3)
	v_mfma_f32_32x32x16_f16 a[16:31], v[14:17], v[18:21], a[16:31]
	s_waitcnt lgkmcnt(1)
	v_mfma_f32_32x32x16_f16 a[0:15], v[14:17], v[28:31], a[0:15]
	v_mfma_f32_32x32x16_f16 a[16:31], v[14:17], v[24:27], a[16:31]
	s_waitcnt lgkmcnt(0)
	v_mfma_f32_32x32x16_f16 a[0:15], v[14:17], v[32:35], a[0:15]
	ds_read_b128 v[18:21], v23 offset:1024
	ds_read_b128 v[24:27], v23 offset:9216
	ds_read_b128 v[28:31], v23 offset:5120
	ds_read_b128 v[32:35], v23 offset:13312
	s_waitcnt lgkmcnt(3)
	v_mfma_f32_32x32x16_f16 a[16:31], v[10:13], v[18:21], a[16:31]
	s_waitcnt lgkmcnt(1)
	v_mfma_f32_32x32x16_f16 a[0:15], v[10:13], v[28:31], a[0:15]
	v_mfma_f32_32x32x16_f16 a[16:31], v[10:13], v[24:27], a[16:31]
	s_waitcnt lgkmcnt(0)
	v_mfma_f32_32x32x16_f16 a[0:15], v[10:13], v[32:35], a[0:15]
	ds_read_b128 v[18:21], v23 offset:2048
	ds_read_b128 v[24:27], v23 offset:10240
	ds_read_b128 v[28:31], v23 offset:6144
	ds_read_b128 v[32:35], v23 offset:14336
	s_waitcnt lgkmcnt(3)
	v_mfma_f32_32x32x16_f16 a[16:31], v[6:9], v[18:21], a[16:31]
	s_waitcnt lgkmcnt(1)
	v_mfma_f32_32x32x16_f16 a[0:15], v[6:9], v[28:31], a[0:15]
	v_mfma_f32_32x32x16_f16 a[16:31], v[6:9], v[24:27], a[16:31]
	s_waitcnt lgkmcnt(0)
	v_mfma_f32_32x32x16_f16 a[0:15], v[6:9], v[32:35], a[0:15]
	ds_read_b128 v[18:21], v23 offset:3072
	ds_read_b128 v[24:27], v23 offset:11264
	ds_read_b128 v[28:31], v23 offset:7168
	ds_read_b128 v[32:35], v23 offset:15360
	s_waitcnt lgkmcnt(3)
	v_mfma_f32_32x32x16_f16 a[16:31], v[2:5], v[18:21], a[16:31]
	s_waitcnt lgkmcnt(1)
	v_mfma_f32_32x32x16_f16 a[0:15], v[2:5], v[28:31], a[0:15]
	v_mfma_f32_32x32x16_f16 a[16:31], v[2:5], v[24:27], a[16:31]
	s_waitcnt lgkmcnt(0)
	v_mfma_f32_32x32x16_f16 a[0:15], v[2:5], v[32:35], a[0:15]
	ds_read_b128 v[18:21], v23 offset:16384
	ds_read_b128 v[24:27], v23 offset:24576
	ds_read_b128 v[28:31], v23 offset:20480
	ds_read_b128 v[32:35], v23 offset:28672
	s_waitcnt lgkmcnt(3)
	v_mfma_f32_32x32x16_f16 a[32:47], v[14:17], v[18:21], 0
	s_waitcnt lgkmcnt(1)
	v_mfma_f32_32x32x16_f16 a[48:63], v[14:17], v[28:31], 0
	v_mfma_f32_32x32x16_f16 a[32:47], v[14:17], v[24:27], a[32:47]
	s_waitcnt lgkmcnt(0)
	v_mfma_f32_32x32x16_f16 a[48:63], v[14:17], v[32:35], a[48:63]
	ds_read_b128 v[14:17], v23 offset:17408
	ds_read_b128 v[18:21], v23 offset:25600
	ds_read_b128 v[24:27], v23 offset:21504
	ds_read_b128 v[28:31], v23 offset:29696
	s_waitcnt lgkmcnt(3)
	v_mfma_f32_32x32x16_f16 a[32:47], v[10:13], v[14:17], a[32:47]
	s_waitcnt lgkmcnt(1)
	v_mfma_f32_32x32x16_f16 a[48:63], v[10:13], v[24:27], a[48:63]
	v_mfma_f32_32x32x16_f16 a[32:47], v[10:13], v[18:21], a[32:47]
	s_waitcnt lgkmcnt(0)
	v_mfma_f32_32x32x16_f16 a[48:63], v[10:13], v[28:31], a[48:63]
	ds_read_b128 v[10:13], v23 offset:18432
	ds_read_b128 v[14:17], v23 offset:26624
	ds_read_b128 v[18:21], v23 offset:22528
	ds_read_b128 v[24:27], v23 offset:30720
	s_waitcnt lgkmcnt(3)
	v_mfma_f32_32x32x16_f16 a[32:47], v[6:9], v[10:13], a[32:47]
	s_waitcnt lgkmcnt(1)
	v_mfma_f32_32x32x16_f16 a[48:63], v[6:9], v[18:21], a[48:63]
	v_mfma_f32_32x32x16_f16 a[32:47], v[6:9], v[14:17], a[32:47]
	s_waitcnt lgkmcnt(0)
	v_mfma_f32_32x32x16_f16 a[48:63], v[6:9], v[24:27], a[48:63]
	ds_read_b128 v[10:13], v23 offset:19456
	ds_read_b128 v[6:9], v23 offset:27648
	ds_read_b128 v[18:21], v23 offset:23552
	ds_read_b128 v[14:17], v23 offset:31744
	s_waitcnt lgkmcnt(3)
	v_mfma_f32_32x32x16_f16 a[32:47], v[2:5], v[10:13], a[32:47]
	s_waitcnt lgkmcnt(1)
	v_mfma_f32_32x32x16_f16 a[48:63], v[2:5], v[18:21], a[48:63]
	v_mfma_f32_32x32x16_f16 a[32:47], v[2:5], v[6:9], a[32:47]
	v_lshlrev_b32_e32 v7, 2, v22
	s_waitcnt lgkmcnt(0)
	v_mfma_f32_32x32x16_f16 a[48:63], v[2:5], v[14:17], a[48:63]
	v_accvgpr_read_b32 v2, a0
	v_accvgpr_read_b32 v3, a16
	v_cvt_pk_bf16_f32 v6, v3, v2
	v_lshlrev_b64 v[2:3], 7, v[0:1]
	v_or_b32_e32 v2, v2, v7
	v_lshl_add_u64 v[4:5], s[6:7], 0, v[2:3]
	global_store_dword v[4:5], v6, off
	s_nop 1
	v_accvgpr_read_b32 v4, a32
	v_lshl_add_u64 v[2:3], s[2:3], 0, v[2:3]
	s_nop 0
	v_accvgpr_read_b32 v1, a48
	v_cvt_pk_bf16_f32 v1, v4, v1
	global_store_dword v[2:3], v1, off
	v_or_b32_e32 v2, 1, v0
	v_ashrrev_i32_e32 v3, 31, v2
	v_lshlrev_b64 v[2:3], 7, v[2:3]
	v_accvgpr_read_b32 v1, a1
	v_accvgpr_read_b32 v4, a17
	v_or_b32_e32 v2, v2, v7
	v_cvt_pk_bf16_f32 v1, v4, v1
	v_lshl_add_u64 v[4:5], s[6:7], 0, v[2:3]
	global_store_dword v[4:5], v1, off
	v_accvgpr_read_b32 v1, a49
	v_accvgpr_read_b32 v4, a33
	v_cvt_pk_bf16_f32 v1, v4, v1
	v_lshl_add_u64 v[2:3], s[2:3], 0, v[2:3]
	global_store_dword v[2:3], v1, off
	v_or_b32_e32 v2, 2, v0
	v_ashrrev_i32_e32 v3, 31, v2
	v_lshlrev_b64 v[2:3], 7, v[2:3]
	v_accvgpr_read_b32 v1, a2
	v_accvgpr_read_b32 v4, a18
	v_or_b32_e32 v2, v2, v7
	v_cvt_pk_bf16_f32 v1, v4, v1
	v_lshl_add_u64 v[4:5], s[6:7], 0, v[2:3]
	global_store_dword v[4:5], v1, off
	v_accvgpr_read_b32 v1, a50
	v_accvgpr_read_b32 v4, a34
	v_cvt_pk_bf16_f32 v1, v4, v1
	v_lshl_add_u64 v[2:3], s[2:3], 0, v[2:3]
	global_store_dword v[2:3], v1, off
	v_or_b32_e32 v2, 3, v0
	v_ashrrev_i32_e32 v3, 31, v2
	v_lshlrev_b64 v[2:3], 7, v[2:3]
	v_accvgpr_read_b32 v1, a3
	v_accvgpr_read_b32 v4, a19
	v_or_b32_e32 v2, v2, v7
	v_cvt_pk_bf16_f32 v1, v4, v1
	v_lshl_add_u64 v[4:5], s[6:7], 0, v[2:3]
	global_store_dword v[4:5], v1, off
	v_accvgpr_read_b32 v1, a51
	v_accvgpr_read_b32 v4, a35
	v_cvt_pk_bf16_f32 v1, v4, v1
	v_lshl_add_u64 v[2:3], s[2:3], 0, v[2:3]
	global_store_dword v[2:3], v1, off
	v_or_b32_e32 v2, 8, v0
	v_ashrrev_i32_e32 v3, 31, v2
	v_lshlrev_b64 v[2:3], 7, v[2:3]
	v_accvgpr_read_b32 v1, a4
	v_accvgpr_read_b32 v4, a20
	v_or_b32_e32 v2, v2, v7
	v_cvt_pk_bf16_f32 v1, v4, v1
	v_lshl_add_u64 v[4:5], s[6:7], 0, v[2:3]
	global_store_dword v[4:5], v1, off
	v_accvgpr_read_b32 v1, a52
	v_accvgpr_read_b32 v4, a36
	v_cvt_pk_bf16_f32 v1, v4, v1
	v_lshl_add_u64 v[2:3], s[2:3], 0, v[2:3]
	global_store_dword v[2:3], v1, off
	v_or_b32_e32 v2, 9, v0
	v_ashrrev_i32_e32 v3, 31, v2
	v_lshlrev_b64 v[2:3], 7, v[2:3]
	v_accvgpr_read_b32 v1, a5
	v_accvgpr_read_b32 v4, a21
	v_or_b32_e32 v2, v2, v7
	v_cvt_pk_bf16_f32 v1, v4, v1
	v_lshl_add_u64 v[4:5], s[6:7], 0, v[2:3]
	global_store_dword v[4:5], v1, off
	v_accvgpr_read_b32 v1, a53
	v_accvgpr_read_b32 v4, a37
	v_cvt_pk_bf16_f32 v1, v4, v1
	v_lshl_add_u64 v[2:3], s[2:3], 0, v[2:3]
	global_store_dword v[2:3], v1, off
	v_or_b32_e32 v2, 10, v0
	v_ashrrev_i32_e32 v3, 31, v2
	v_lshlrev_b64 v[2:3], 7, v[2:3]
	v_accvgpr_read_b32 v1, a6
	v_accvgpr_read_b32 v4, a22
	v_or_b32_e32 v2, v2, v7
	v_cvt_pk_bf16_f32 v1, v4, v1
	v_lshl_add_u64 v[4:5], s[6:7], 0, v[2:3]
	global_store_dword v[4:5], v1, off
	v_accvgpr_read_b32 v1, a54
	v_accvgpr_read_b32 v4, a38
	v_cvt_pk_bf16_f32 v1, v4, v1
	v_lshl_add_u64 v[2:3], s[2:3], 0, v[2:3]
	global_store_dword v[2:3], v1, off
	v_or_b32_e32 v2, 11, v0
	v_ashrrev_i32_e32 v3, 31, v2
	v_lshlrev_b64 v[2:3], 7, v[2:3]
	v_accvgpr_read_b32 v1, a7
	v_accvgpr_read_b32 v4, a23
	v_or_b32_e32 v2, v2, v7
	v_cvt_pk_bf16_f32 v1, v4, v1
	v_lshl_add_u64 v[4:5], s[6:7], 0, v[2:3]
	global_store_dword v[4:5], v1, off
	v_accvgpr_read_b32 v1, a55
	v_accvgpr_read_b32 v4, a39
	v_cvt_pk_bf16_f32 v1, v4, v1
	v_lshl_add_u64 v[2:3], s[2:3], 0, v[2:3]
	global_store_dword v[2:3], v1, off
	v_or_b32_e32 v2, 16, v0
	v_ashrrev_i32_e32 v3, 31, v2
	v_lshlrev_b64 v[2:3], 7, v[2:3]
	v_accvgpr_read_b32 v1, a8
	v_accvgpr_read_b32 v4, a24
	v_or_b32_e32 v2, v2, v7
	v_cvt_pk_bf16_f32 v1, v4, v1
	v_lshl_add_u64 v[4:5], s[6:7], 0, v[2:3]
	global_store_dword v[4:5], v1, off
	v_accvgpr_read_b32 v1, a56
	v_accvgpr_read_b32 v4, a40
	v_cvt_pk_bf16_f32 v1, v4, v1
	v_lshl_add_u64 v[2:3], s[2:3], 0, v[2:3]
	global_store_dword v[2:3], v1, off
	v_or_b32_e32 v2, 17, v0
	v_ashrrev_i32_e32 v3, 31, v2
	v_lshlrev_b64 v[2:3], 7, v[2:3]
	v_accvgpr_read_b32 v1, a9
	v_accvgpr_read_b32 v4, a25
	v_or_b32_e32 v2, v2, v7
	v_cvt_pk_bf16_f32 v1, v4, v1
	v_lshl_add_u64 v[4:5], s[6:7], 0, v[2:3]
	global_store_dword v[4:5], v1, off
	v_accvgpr_read_b32 v1, a57
	v_accvgpr_read_b32 v4, a41
	v_cvt_pk_bf16_f32 v1, v4, v1
	v_lshl_add_u64 v[2:3], s[2:3], 0, v[2:3]
	global_store_dword v[2:3], v1, off
	v_or_b32_e32 v2, 18, v0
	v_ashrrev_i32_e32 v3, 31, v2
	v_lshlrev_b64 v[2:3], 7, v[2:3]
	v_accvgpr_read_b32 v1, a10
	v_accvgpr_read_b32 v4, a26
	v_or_b32_e32 v2, v2, v7
	v_cvt_pk_bf16_f32 v1, v4, v1
	v_lshl_add_u64 v[4:5], s[6:7], 0, v[2:3]
	global_store_dword v[4:5], v1, off
	v_accvgpr_read_b32 v1, a58
	v_accvgpr_read_b32 v4, a42
	v_cvt_pk_bf16_f32 v1, v4, v1
	v_lshl_add_u64 v[2:3], s[2:3], 0, v[2:3]
	global_store_dword v[2:3], v1, off
	v_or_b32_e32 v2, 19, v0
	v_ashrrev_i32_e32 v3, 31, v2
	v_lshlrev_b64 v[2:3], 7, v[2:3]
	v_accvgpr_read_b32 v1, a11
	v_accvgpr_read_b32 v4, a27
	v_or_b32_e32 v2, v2, v7
	v_cvt_pk_bf16_f32 v1, v4, v1
	v_lshl_add_u64 v[4:5], s[6:7], 0, v[2:3]
	global_store_dword v[4:5], v1, off
	v_accvgpr_read_b32 v1, a59
	v_accvgpr_read_b32 v4, a43
	v_cvt_pk_bf16_f32 v1, v4, v1
	v_lshl_add_u64 v[2:3], s[2:3], 0, v[2:3]
	global_store_dword v[2:3], v1, off
	v_or_b32_e32 v2, 24, v0
	v_ashrrev_i32_e32 v3, 31, v2
	v_lshlrev_b64 v[2:3], 7, v[2:3]
	v_accvgpr_read_b32 v1, a12
	v_accvgpr_read_b32 v4, a28
	v_or_b32_e32 v2, v2, v7
	v_cvt_pk_bf16_f32 v1, v4, v1
	v_lshl_add_u64 v[4:5], s[6:7], 0, v[2:3]
	global_store_dword v[4:5], v1, off
	v_accvgpr_read_b32 v1, a60
	v_accvgpr_read_b32 v4, a44
	v_cvt_pk_bf16_f32 v1, v4, v1
	v_lshl_add_u64 v[2:3], s[2:3], 0, v[2:3]
	global_store_dword v[2:3], v1, off
	v_or_b32_e32 v2, 25, v0
	v_ashrrev_i32_e32 v3, 31, v2
	v_lshlrev_b64 v[2:3], 7, v[2:3]
	v_accvgpr_read_b32 v1, a13
	v_accvgpr_read_b32 v4, a29
	v_or_b32_e32 v2, v2, v7
	v_cvt_pk_bf16_f32 v1, v4, v1
	v_lshl_add_u64 v[4:5], s[6:7], 0, v[2:3]
	global_store_dword v[4:5], v1, off
	v_accvgpr_read_b32 v1, a61
	v_accvgpr_read_b32 v4, a45
	v_cvt_pk_bf16_f32 v1, v4, v1
	v_lshl_add_u64 v[2:3], s[2:3], 0, v[2:3]
	global_store_dword v[2:3], v1, off
	v_or_b32_e32 v2, 26, v0
	v_ashrrev_i32_e32 v3, 31, v2
	v_lshlrev_b64 v[2:3], 7, v[2:3]
	v_accvgpr_read_b32 v1, a14
	v_accvgpr_read_b32 v4, a30
	v_or_b32_e32 v2, v2, v7
	v_cvt_pk_bf16_f32 v1, v4, v1
	v_lshl_add_u64 v[4:5], s[6:7], 0, v[2:3]
	global_store_dword v[4:5], v1, off
	v_accvgpr_read_b32 v1, a62
	v_accvgpr_read_b32 v4, a46
	v_cvt_pk_bf16_f32 v1, v4, v1
	v_lshl_add_u64 v[2:3], s[2:3], 0, v[2:3]
	v_or_b32_e32 v0, 27, v0
	global_store_dword v[2:3], v1, off
	v_ashrrev_i32_e32 v1, 31, v0
	v_lshlrev_b64 v[0:1], 7, v[0:1]
	v_accvgpr_read_b32 v2, a15
	v_accvgpr_read_b32 v3, a31
	v_or_b32_e32 v0, v0, v7
	v_cvt_pk_bf16_f32 v4, v3, v2
	v_lshl_add_u64 v[2:3], s[6:7], 0, v[0:1]
	global_store_dword v[2:3], v4, off
	v_accvgpr_read_b32 v2, a63
	v_accvgpr_read_b32 v3, a47
	v_cvt_pk_bf16_f32 v2, v3, v2
	v_lshl_add_u64 v[0:1], s[2:3], 0, v[0:1]
	global_store_dword v[0:1], v2, off

amdhsa.kernels:
  - .agpr_count:     0
    .args:
      - .actual_access:  read_only
        .address_space:  global
        .offset:         0
        .size:           8
        .value_kind:     global_buffer
      - .actual_access:  read_only
        .address_space:  global
        .offset:         8
        .size:           8
        .value_kind:     global_buffer
      - .actual_access:  read_only
        .address_space:  global
        .offset:         16
        .size:           8
        .value_kind:     global_buffer
      - .actual_access:  read_only
        .address_space:  global
        .offset:         24
        .size:           8
        .value_kind:     global_buffer
      - .actual_access:  write_only
        .address_space:  global
        .offset:         32
        .size:           8
        .value_kind:     global_buffer
      - .actual_access:  write_only
        .address_space:  global
        .offset:         40
        .size:           8
        .value_kind:     global_buffer
      - .actual_access:  write_only
        .address_space:  global
        .offset:         48
        .size:           8
        .value_kind:     global_buffer
      - .offset:         56
        .size:           4
        .value_kind:     hidden_block_count_x
      - .offset:         60
        .size:           4
        .value_kind:     hidden_block_count_y
      - .offset:         64
        .size:           4
        .value_kind:     hidden_block_count_z
      - .offset:         68
        .size:           2
        .value_kind:     hidden_group_size_x
      - .offset:         70
        .size:           2
        .value_kind:     hidden_group_size_y
      - .offset:         72
        .size:           2
        .value_kind:     hidden_group_size_z
      - .offset:         74
        .size:           2
        .value_kind:     hidden_remainder_x
      - .offset:         76
        .size:           2
        .value_kind:     hidden_remainder_y
      - .offset:         78
        .size:           2
        .value_kind:     hidden_remainder_z
      - .offset:         96
        .size:           8
        .value_kind:     hidden_global_offset_x
      - .offset:         104
        .size:           8
        .value_kind:     hidden_global_offset_y
      - .offset:         112
        .size:           8
        .value_kind:     hidden_global_offset_z
      - .offset:         120
        .size:           2
        .value_kind:     hidden_grid_dims
    .group_segment_fixed_size: 0
    .kernarg_segment_align: 8
    .kernarg_segment_size: 312
    .language:       OpenCL C
    .language_version:
      - 2
      - 0
    .max_flat_workgroup_size: 256
    .name:           _Z6k_prepPKfS0_S0_S0_P15HIP_vector_typeIjLj4EEPiPd
    .private_segment_fixed_size: 0
    .sgpr_count:     25
    .sgpr_spill_count: 0
    .symbol:         _Z6k_prepPKfS0_S0_S0_P15HIP_vector_typeIjLj4EEPiPd.kd
    .uniform_work_group_size: 1
    .uses_dynamic_stack: false
    .vgpr_count:     24
    .vgpr_spill_count: 0
    .wavefront_size: 64
  - .agpr_count:     0
    .args:
      - .actual_access:  read_only
        .address_space:  global
        .offset:         0
        .size:           8
        .value_kind:     global_buffer
      - .actual_access:  read_only
        .address_space:  global
        .offset:         8
        .size:           8
        .value_kind:     global_buffer
      - .actual_access:  read_only
        .address_space:  global
        .offset:         16
        .size:           8
        .value_kind:     global_buffer
      - .actual_access:  read_only
        .address_space:  global
        .offset:         24
        .size:           8
        .value_kind:     global_buffer
      - .actual_access:  read_only
        .address_space:  global
        .offset:         32
        .size:           8
        .value_kind:     global_buffer
      - .actual_access:  write_only
        .address_space:  global
        .offset:         40
        .size:           8
        .value_kind:     global_buffer
      - .actual_access:  write_only
        .address_space:  global
        .offset:         48
        .size:           8
        .value_kind:     global_buffer
    .group_segment_fixed_size: 4112
    .kernarg_segment_align: 8
    .kernarg_segment_size: 56
    .language:       OpenCL C
    .language_version:
      - 2
      - 0
    .max_flat_workgroup_size: 256
    .name:           _Z10k_bscatterPKiS0_PKfS0_S0_PiP15HIP_vector_typeIjLj2EE
    .private_segment_fixed_size: 0
    .sgpr_count:     28
    .sgpr_spill_count: 0
    .symbol:         _Z10k_bscatterPKiS0_PKfS0_S0_PiP15HIP_vector_typeIjLj2EE.kd
    .uniform_work_group_size: 1
    .uses_dynamic_stack: false
    .vgpr_count:     78
    .vgpr_spill_count: 0
    .wavefront_size: 64
  - .agpr_count:     0
    .args:
      - .actual_access:  read_only
        .address_space:  global
        .offset:         0
        .size:           8
        .value_kind:     global_buffer
      - .actual_access:  read_only
        .address_space:  global
        .offset:         8
        .size:           8
        .value_kind:     global_buffer
      - .actual_access:  write_only
        .address_space:  global
        .offset:         16
        .size:           8
        .value_kind:     global_buffer
      - .actual_access:  write_only
        .address_space:  global
        .offset:         24
        .size:           8
        .value_kind:     global_buffer
      - .actual_access:  write_only
        .address_space:  global
        .offset:         32
        .size:           8
        .value_kind:     global_buffer
      - .actual_access:  write_only
        .address_space:  global
        .offset:         40
        .size:           8
        .value_kind:     global_buffer
    .group_segment_fixed_size: 29200
    .kernarg_segment_align: 8
    .kernarg_segment_size: 48
    .language:       OpenCL C
    .language_version:
      - 2
      - 0
    .max_flat_workgroup_size: 256
    .name:           _Z7k_bsortPKiPK15HIP_vector_typeIjLj2EEPiS5_S5_Pf
    .private_segment_fixed_size: 0
    .sgpr_count:     106
    .sgpr_spill_count: 12
    .symbol:         _Z7k_bsortPKiPK15HIP_vector_typeIjLj2EEPiS5_S5_Pf.kd
    .uniform_work_group_size: 1
    .uses_dynamic_stack: false
    .vgpr_count:     69
    .vgpr_spill_count: 0
    .wavefront_size: 64
  - .agpr_count:     32
    .args:
      - .address_space:  global
        .offset:         0
        .size:           8
        .value_kind:     global_buffer
      - .actual_access:  read_only
        .address_space:  global
        .offset:         8
        .size:           8
        .value_kind:     global_buffer
      - .actual_access:  read_only
        .address_space:  global
        .offset:         16
        .size:           8
        .value_kind:     global_buffer
      - .actual_access:  read_only
        .address_space:  global
        .offset:         24
        .size:           8
        .value_kind:     global_buffer
      - .actual_access:  read_only
        .address_space:  global
        .offset:         32
        .size:           8
        .value_kind:     global_buffer
      - .actual_access:  read_only
        .address_space:  global
        .offset:         40
        .size:           8
        .value_kind:     global_buffer
      - .address_space:  global
        .offset:         48
        .size:           8
        .value_kind:     global_buffer
      - .address_space:  global
        .offset:         56
        .size:           8
        .value_kind:     global_buffer
      - .offset:         64
        .size:           4
        .value_kind:     hidden_block_count_x
      - .offset:         68
        .size:           4
        .value_kind:     hidden_block_count_y
      - .offset:         72
        .size:           4
        .value_kind:     hidden_block_count_z
      - .offset:         76
        .size:           2
        .value_kind:     hidden_group_size_x
      - .offset:         78
        .size:           2
        .value_kind:     hidden_group_size_y
      - .offset:         80
        .size:           2
        .value_kind:     hidden_group_size_z
      - .offset:         82
        .size:           2
        .value_kind:     hidden_remainder_x
      - .offset:         84
        .size:           2
        .value_kind:     hidden_remainder_y
      - .offset:         86
        .size:           2
        .value_kind:     hidden_remainder_z
      - .offset:         104
        .size:           8
        .value_kind:     hidden_global_offset_x
      - .offset:         112
        .size:           8
        .value_kind:     hidden_global_offset_y
      - .offset:         120
        .size:           8
        .value_kind:     hidden_global_offset_z
      - .offset:         128
        .size:           2
        .value_kind:     hidden_grid_dims
    .group_segment_fixed_size: 18944
    .kernarg_segment_align: 8
    .kernarg_segment_size: 320
    .language:       OpenCL C
    .language_version:
      - 2
      - 0
    .max_flat_workgroup_size: 256
    .name:           _Z4k_U2PKtPK15HIP_vector_typeIjLj4EEPKdPKfS8_S8_PtPd
    .private_segment_fixed_size: 0
    .sgpr_count:     30
    .sgpr_spill_count: 0
    .symbol:         _Z4k_U2PKtPK15HIP_vector_typeIjLj4EEPKdPKfS8_S8_PtPd.kd
    .uniform_work_group_size: 1
    .uses_dynamic_stack: false
    .vgpr_count:     104
    .vgpr_spill_count: 0
    .wavefront_size: 64
  - .agpr_count:     0
    .args:
      - .actual_access:  read_only
        .address_space:  global
        .offset:         0
        .size:           8
        .value_kind:     global_buffer
      - .actual_access:  read_only
        .address_space:  global
        .offset:         8
        .size:           8
        .value_kind:     global_buffer
      - .actual_access:  write_only
        .address_space:  global
        .offset:         16
        .size:           8
        .value_kind:     global_buffer
    .group_segment_fixed_size: 0
    .kernarg_segment_align: 8
    .kernarg_segment_size: 24
    .language:       OpenCL C
    .language_version:
      - 2
      - 0
    .max_flat_workgroup_size: 1024
    .name:           _Z7k_finalPKdPKfPf
    .private_segment_fixed_size: 0
    .sgpr_count:     28
    .sgpr_spill_count: 0
    .symbol:         _Z7k_finalPKdPKfPf.kd
    .uniform_work_group_size: 1
    .uses_dynamic_stack: false
    .vgpr_count:     10
    .vgpr_spill_count: 0
    .wavefront_size: 64
  - .agpr_count:     64
    .args:
      - .actual_access:  read_only
        .address_space:  global
        .offset:         0
        .size:           8
        .value_kind:     global_buffer
      - .address_space:  global
        .offset:         8
        .size:           8
        .value_kind:     global_buffer
      - .actual_access:  write_only
        .address_space:  global
        .offset:         16
        .size:           8
        .value_kind:     global_buffer
      - .actual_access:  read_only
        .address_space:  global
        .offset:         24
        .size:           8
        .value_kind:     global_buffer
      - .actual_access:  read_only
        .address_space:  global
        .offset:         32
        .size:           8
        .value_kind:     global_buffer
      - .actual_access:  read_only
        .address_space:  global
        .offset:         40
        .size:           8
        .value_kind:     global_buffer
      - .actual_access:  read_only
        .address_space:  global
        .offset:         48
        .size:           8
        .value_kind:     global_buffer
      - .actual_access:  read_only
        .address_space:  global
        .offset:         56
        .size:           8
        .value_kind:     global_buffer
      - .actual_access:  write_only
        .address_space:  global
        .offset:         64
        .size:           8
        .value_kind:     global_buffer
      - .actual_access:  write_only
        .address_space:  global
        .offset:         72
        .size:           8
        .value_kind:     global_buffer
      - .actual_access:  write_only
        .address_space:  global
        .offset:         80
        .size:           8
        .value_kind:     global_buffer
      - .offset:         88
        .size:           4
        .value_kind:     hidden_block_count_x
      - .offset:         92
        .size:           4
        .value_kind:     hidden_block_count_y
      - .offset:         96
        .size:           4
        .value_kind:     hidden_block_count_z
      - .offset:         100
        .size:           2
        .value_kind:     hidden_group_size_x
      - .offset:         102
        .size:           2
        .value_kind:     hidden_group_size_y
      - .offset:         104
        .size:           2
        .value_kind:     hidden_group_size_z
      - .offset:         106
        .size:           2
        .value_kind:     hidden_remainder_x
      - .offset:         108
        .size:           2
        .value_kind:     hidden_remainder_y
      - .offset:         110
        .size:           2
        .value_kind:     hidden_remainder_z
      - .offset:         128
        .size:           8
        .value_kind:     hidden_global_offset_x
      - .offset:         136
        .size:           8
        .value_kind:     hidden_global_offset_y
      - .offset:         144
        .size:           8
        .value_kind:     hidden_global_offset_z
      - .offset:         152
        .size:           2
        .value_kind:     hidden_grid_dims
    .group_segment_fixed_size: 45312
    .kernarg_segment_align: 8
    .kernarg_segment_size: 344
    .language:       OpenCL C
    .language_version:
      - 2
      - 0
    .max_flat_workgroup_size: 256
    .name:           _Z14k_bcount_node0ItEvPKiPiS2_PKfS4_S4_S4_PK15HIP_vector_typeIjLj4EEPtPT_SB_
    .private_segment_fixed_size: 0
    .sgpr_count:     26
    .sgpr_spill_count: 0
    .symbol:         _Z14k_bcount_node0ItEvPKiPiS2_PKfS4_S4_S4_PK15HIP_vector_typeIjLj4EEPtPT_SB_.kd
    .uniform_work_group_size: 1
    .uses_dynamic_stack: false
    .vgpr_count:     232
    .vgpr_spill_count: 0
    .wavefront_size: 64
  - .agpr_count:     0
    .args:
      - .actual_access:  read_only
        .address_space:  global
        .offset:         0
        .size:           8
        .value_kind:     global_buffer
      - .actual_access:  read_only
        .address_space:  global
        .offset:         8
        .size:           8
        .value_kind:     global_buffer
      - .actual_access:  read_only
        .address_space:  global
        .offset:         16
        .size:           8
        .value_kind:     global_buffer
      - .actual_access:  read_only
        .address_space:  global
        .offset:         24
        .size:           8
        .value_kind:     global_buffer
      - .actual_access:  read_only
        .address_space:  global
        .offset:         32
        .size:           8
        .value_kind:     global_buffer
      - .actual_access:  read_only
        .address_space:  global
        .offset:         40
        .size:           8
        .value_kind:     global_buffer
      - .address_space:  global
        .offset:         48
        .size:           8
        .value_kind:     global_buffer
      - .offset:         56
        .size:           4
        .value_kind:     hidden_block_count_x
      - .offset:         60
        .size:           4
        .value_kind:     hidden_block_count_y
      - .offset:         64
        .size:           4
        .value_kind:     hidden_block_count_z
      - .offset:         68
        .size:           2
        .value_kind:     hidden_group_size_x
      - .offset:         70
        .size:           2
        .value_kind:     hidden_group_size_y
      - .offset:         72
        .size:           2
        .value_kind:     hidden_group_size_z
      - .offset:         74
        .size:           2
        .value_kind:     hidden_remainder_x
      - .offset:         76
        .size:           2
        .value_kind:     hidden_remainder_y
      - .offset:         78
        .size:           2
        .value_kind:     hidden_remainder_z
      - .offset:         96
        .size:           8
        .value_kind:     hidden_global_offset_x
      - .offset:         104
        .size:           8
        .value_kind:     hidden_global_offset_y
      - .offset:         112
        .size:           8
        .value_kind:     hidden_global_offset_z
      - .offset:         120
        .size:           2
        .value_kind:     hidden_grid_dims
    .group_segment_fixed_size: 2048
    .kernarg_segment_align: 8
    .kernarg_segment_size: 312
    .language:       OpenCL C
    .language_version:
      - 2
      - 0
    .max_flat_workgroup_size: 256
    .name:           _Z7k_passAItEvPKiS1_PKfPKT_S6_S3_Pd
    .private_segment_fixed_size: 0
    .sgpr_count:     36
    .sgpr_spill_count: 0
    .symbol:         _Z7k_passAItEvPKiS1_PKfPKT_S6_S3_Pd.kd
    .uniform_work_group_size: 1
    .uses_dynamic_stack: false
    .vgpr_count:     104
    .vgpr_spill_count: 0
    .wavefront_size: 64
  - .agpr_count:     0
    .args:
      - .actual_access:  read_only
        .address_space:  global
        .offset:         0
        .size:           8
        .value_kind:     global_buffer
      - .actual_access:  read_only
        .address_space:  global
        .offset:         8
        .size:           8
        .value_kind:     global_buffer
      - .actual_access:  read_only
        .address_space:  global
        .offset:         16
        .size:           8
        .value_kind:     global_buffer
      - .actual_access:  read_only
        .address_space:  global
        .offset:         24
        .size:           8
        .value_kind:     global_buffer
      - .actual_access:  read_only
        .address_space:  global
        .offset:         32
        .size:           8
        .value_kind:     global_buffer
      - .actual_access:  read_only
        .address_space:  global
        .offset:         40
        .size:           8
        .value_kind:     global_buffer
      - .actual_access:  read_only
        .address_space:  global
        .offset:         48
        .size:           8
        .value_kind:     global_buffer
      - .actual_access:  read_only
        .address_space:  global
        .offset:         56
        .size:           8
        .value_kind:     global_buffer
      - .actual_access:  read_only
        .address_space:  global
        .offset:         64
        .size:           8
        .value_kind:     global_buffer
      - .actual_access:  read_only
        .address_space:  global
        .offset:         72
        .size:           8
        .value_kind:     global_buffer
      - .actual_access:  read_only
        .address_space:  global
        .offset:         80
        .size:           8
        .value_kind:     global_buffer
      - .actual_access:  read_only
        .address_space:  global
        .offset:         88
        .size:           8
        .value_kind:     global_buffer
      - .actual_access:  read_only
        .address_space:  global
        .offset:         96
        .size:           8
        .value_kind:     global_buffer
      - .address_space:  global
        .offset:         104
        .size:           8
        .value_kind:     global_buffer
      - .actual_access:  read_only
        .address_space:  global
        .offset:         112
        .size:           8
        .value_kind:     global_buffer
      - .actual_access:  read_only
        .address_space:  global
        .offset:         120
        .size:           8
        .value_kind:     global_buffer
      - .address_space:  global
        .offset:         128
        .size:           8
        .value_kind:     global_buffer
      - .offset:         136
        .size:           4
        .value_kind:     hidden_block_count_x
      - .offset:         140
        .size:           4
        .value_kind:     hidden_block_count_y
      - .offset:         144
        .size:           4
        .value_kind:     hidden_block_count_z
      - .offset:         148
        .size:           2
        .value_kind:     hidden_group_size_x
      - .offset:         150
        .size:           2
        .value_kind:     hidden_group_size_y
      - .offset:         152
        .size:           2
        .value_kind:     hidden_group_size_z
      - .offset:         154
        .size:           2
        .value_kind:     hidden_remainder_x
      - .offset:         156
        .size:           2
        .value_kind:     hidden_remainder_y
      - .offset:         158
        .size:           2
        .value_kind:     hidden_remainder_z
      - .offset:         176
        .size:           8
        .value_kind:     hidden_global_offset_x
      - .offset:         184
        .size:           8
        .value_kind:     hidden_global_offset_y
      - .offset:         192
        .size:           8
        .value_kind:     hidden_global_offset_z
      - .offset:         200
        .size:           2
        .value_kind:     hidden_grid_dims
    .group_segment_fixed_size: 37632
    .kernarg_segment_align: 8
    .kernarg_segment_size: 392
    .language:       OpenCL C
    .language_version:
      - 2
      - 0
    .max_flat_workgroup_size: 256
    .name:           _Z7k_passLILi1ELi0ELi1EEvPKiS1_PKfPKtS5_S3_S3_S3_S3_S3_S3_PK15HIP_vector_typeIjLj4EEPKdPdS1_PtS1_
    .private_segment_fixed_size: 0
    .sgpr_count:     62
    .sgpr_spill_count: 0
    .symbol:         _Z7k_passLILi1ELi0ELi1EEvPKiS1_PKfPKtS5_S3_S3_S3_S3_S3_S3_PK15HIP_vector_typeIjLj4EEPKdPdS1_PtS1_.kd
    .uniform_work_group_size: 1
    .uses_dynamic_stack: false
    .vgpr_count:     128
    .vgpr_spill_count: 0
    .wavefront_size: 64
  - .agpr_count:     0
    .args:
      - .actual_access:  read_only
        .address_space:  global
        .offset:         0
        .size:           8
        .value_kind:     global_buffer
      - .actual_access:  read_only
        .address_space:  global
        .offset:         8
        .size:           8
        .value_kind:     global_buffer
      - .actual_access:  read_only
        .address_space:  global
        .offset:         16
        .size:           8
        .value_kind:     global_buffer
      - .actual_access:  read_only
        .address_space:  global
        .offset:         24
        .size:           8
        .value_kind:     global_buffer
      - .actual_access:  read_only
        .address_space:  global
        .offset:         32
        .size:           8
        .value_kind:     global_buffer
      - .actual_access:  read_only
        .address_space:  global
        .offset:         40
        .size:           8
        .value_kind:     global_buffer
      - .actual_access:  read_only
        .address_space:  global
        .offset:         48
        .size:           8
        .value_kind:     global_buffer
      - .actual_access:  read_only
        .address_space:  global
        .offset:         56
        .size:           8
        .value_kind:     global_buffer
      - .actual_access:  read_only
        .address_space:  global
        .offset:         64
        .size:           8
        .value_kind:     global_buffer
      - .actual_access:  read_only
        .address_space:  global
        .offset:         72
        .size:           8
        .value_kind:     global_buffer
      - .actual_access:  read_only
        .address_space:  global
        .offset:         80
        .size:           8
        .value_kind:     global_buffer
      - .actual_access:  read_only
        .address_space:  global
        .offset:         88
        .size:           8
        .value_kind:     global_buffer
      - .actual_access:  read_only
        .address_space:  global
        .offset:         96
        .size:           8
        .value_kind:     global_buffer
      - .actual_access:  read_only
        .address_space:  global
        .offset:         104
        .size:           8
        .value_kind:     global_buffer
      - .actual_access:  read_only
        .address_space:  global
        .offset:         112
        .size:           8
        .value_kind:     global_buffer
      - .actual_access:  read_only
        .address_space:  global
        .offset:         120
        .size:           8
        .value_kind:     global_buffer
      - .actual_access:  read_only
        .address_space:  global
        .offset:         128
        .size:           8
        .value_kind:     global_buffer
      - .address_space:  global
        .offset:         136
        .size:           8
        .value_kind:     global_buffer
      - .actual_access:  read_only
        .address_space:  global
        .offset:         144
        .size:           8
        .value_kind:     global_buffer
      - .actual_access:  read_only
        .address_space:  global
        .offset:         152
        .size:           8
        .value_kind:     global_buffer
      - .actual_access:  write_only
        .address_space:  global
        .offset:         160
        .size:           8
        .value_kind:     global_buffer
      - .address_space:  global
        .offset:         168
        .size:           8
        .value_kind:     global_buffer
      - .offset:         176
        .size:           4
        .value_kind:     hidden_block_count_x
      - .offset:         180
        .size:           4
        .value_kind:     hidden_block_count_y
      - .offset:         184
        .size:           4
        .value_kind:     hidden_block_count_z
      - .offset:         188
        .size:           2
        .value_kind:     hidden_group_size_x
      - .offset:         190
        .size:           2
        .value_kind:     hidden_group_size_y
      - .offset:         192
        .size:           2
        .value_kind:     hidden_group_size_z
      - .offset:         194
        .size:           2
        .value_kind:     hidden_remainder_x
      - .offset:         196
        .size:           2
        .value_kind:     hidden_remainder_y
      - .offset:         198
        .size:           2
        .value_kind:     hidden_remainder_z
      - .offset:         216
        .size:           8
        .value_kind:     hidden_global_offset_x
      - .offset:         224
        .size:           8
        .value_kind:     hidden_global_offset_y
      - .offset:         232
        .size:           8
        .value_kind:     hidden_global_offset_z
      - .offset:         240
        .size:           2
        .value_kind:     hidden_grid_dims
    .group_segment_fixed_size: 79104
    .kernarg_segment_align: 8
    .kernarg_segment_size: 432
    .language:       OpenCL C
    .language_version:
      - 2
      - 0
    .max_flat_workgroup_size: 512
    .name:           _Z8k_passCUILi1EEvPKiS1_PKfPKtS5_S3_S3_S3_S3_S3_S3_PK15HIP_vector_typeIjLj4EES9_S9_PKdSB_S1_S1_S5_S3_PtPd
    .private_segment_fixed_size: 0
    .sgpr_count:     35
    .sgpr_spill_count: 0
    .symbol:         _Z8k_passCUILi1EEvPKiS1_PKfPKtS5_S3_S3_S3_S3_S3_S3_PK15HIP_vector_typeIjLj4EES9_S9_PKdSB_S1_S1_S5_S3_PtPd.kd
    .uniform_work_group_size: 1
    .uses_dynamic_stack: false
    .vgpr_count:     128
    .vgpr_spill_count: 0
    .wavefront_size: 64
  - .agpr_count:     64
    .args:
      - .actual_access:  read_only
        .address_space:  global
        .offset:         0
        .size:           8
        .value_kind:     global_buffer
      - .address_space:  global
        .offset:         8
        .size:           8
        .value_kind:     global_buffer
      - .actual_access:  read_only
        .address_space:  global
        .offset:         16
        .size:           8
        .value_kind:     global_buffer
      - .actual_access:  read_only
        .address_space:  global
        .offset:         24
        .size:           8
        .value_kind:     global_buffer
      - .actual_access:  read_only
        .address_space:  global
        .offset:         32
        .size:           8
        .value_kind:     global_buffer
      - .actual_access:  read_only
        .address_space:  global
        .offset:         40
        .size:           8
        .value_kind:     global_buffer
      - .actual_access:  read_only
        .address_space:  global
        .offset:         48
        .size:           8
        .value_kind:     global_buffer
      - .actual_access:  write_only
        .address_space:  global
        .offset:         56
        .size:           8
        .value_kind:     global_buffer
      - .actual_access:  write_only
        .address_space:  global
        .offset:         64
        .size:           8
        .value_kind:     global_buffer
      - .actual_access:  read_only
        .address_space:  global
        .offset:         72
        .size:           8
        .value_kind:     global_buffer
      - .actual_access:  read_only
        .address_space:  global
        .offset:         80
        .size:           8
        .value_kind:     global_buffer
      - .offset:         88
        .size:           4
        .value_kind:     hidden_block_count_x
      - .offset:         92
        .size:           4
        .value_kind:     hidden_block_count_y
      - .offset:         96
        .size:           4
        .value_kind:     hidden_block_count_z
      - .offset:         100
        .size:           2
        .value_kind:     hidden_group_size_x
      - .offset:         102
        .size:           2
        .value_kind:     hidden_group_size_y
      - .offset:         104
        .size:           2
        .value_kind:     hidden_group_size_z
      - .offset:         106
        .size:           2
        .value_kind:     hidden_remainder_x
      - .offset:         108
        .size:           2
        .value_kind:     hidden_remainder_y
      - .offset:         110
        .size:           2
        .value_kind:     hidden_remainder_z
      - .offset:         128
        .size:           8
        .value_kind:     hidden_global_offset_x
      - .offset:         136
        .size:           8
        .value_kind:     hidden_global_offset_y
      - .offset:         144
        .size:           8
        .value_kind:     hidden_global_offset_z
      - .offset:         152
        .size:           2
        .value_kind:     hidden_grid_dims
    .group_segment_fixed_size: 33280
    .kernarg_segment_align: 8
    .kernarg_segment_size: 344
    .language:       OpenCL C
    .language_version:
      - 2
      - 0
    .max_flat_workgroup_size: 256
    .name:           _Z4k_U3ILb0EtEvPKtPtPKdPKfS6_PK15HIP_vector_typeIjLj4EES6_PT0_SC_S6_Pd
    .private_segment_fixed_size: 0
    .sgpr_count:     20
    .sgpr_spill_count: 0
    .symbol:         _Z4k_U3ILb0EtEvPKtPtPKdPKfS6_PK15HIP_vector_typeIjLj4EES6_PT0_SC_S6_Pd.kd
    .uniform_work_group_size: 1
    .uses_dynamic_stack: false
    .vgpr_count:     144
    .vgpr_spill_count: 0
    .wavefront_size: 64
  - .agpr_count:     0
    .args:
      - .actual_access:  read_only
        .address_space:  global
        .offset:         0
        .size:           8
        .value_kind:     global_buffer
      - .actual_access:  read_only
        .address_space:  global
        .offset:         8
        .size:           8
        .value_kind:     global_buffer
      - .actual_access:  read_only
        .address_space:  global
        .offset:         16
        .size:           8
        .value_kind:     global_buffer
      - .actual_access:  read_only
        .address_space:  global
        .offset:         24
        .size:           8
        .value_kind:     global_buffer
      - .actual_access:  read_only
        .address_space:  global
        .offset:         32
        .size:           8
        .value_kind:     global_buffer
      - .actual_access:  read_only
        .address_space:  global
        .offset:         40
        .size:           8
        .value_kind:     global_buffer
      - .actual_access:  read_only
        .address_space:  global
        .offset:         48
        .size:           8
        .value_kind:     global_buffer
      - .actual_access:  read_only
        .address_space:  global
        .offset:         56
        .size:           8
        .value_kind:     global_buffer
      - .actual_access:  read_only
        .address_space:  global
        .offset:         64
        .size:           8
        .value_kind:     global_buffer
      - .actual_access:  read_only
        .address_space:  global
        .offset:         72
        .size:           8
        .value_kind:     global_buffer
      - .address_space:  global
        .offset:         80
        .size:           8
        .value_kind:     global_buffer
      - .offset:         88
        .size:           4
        .value_kind:     hidden_block_count_x
      - .offset:         92
        .size:           4
        .value_kind:     hidden_block_count_y
      - .offset:         96
        .size:           4
        .value_kind:     hidden_block_count_z
      - .offset:         100
        .size:           2
        .value_kind:     hidden_group_size_x
      - .offset:         102
        .size:           2
        .value_kind:     hidden_group_size_y
      - .offset:         104
        .size:           2
        .value_kind:     hidden_group_size_z
      - .offset:         106
        .size:           2
        .value_kind:     hidden_remainder_x
      - .offset:         108
        .size:           2
        .value_kind:     hidden_remainder_y
      - .offset:         110
        .size:           2
        .value_kind:     hidden_remainder_z
      - .offset:         128
        .size:           8
        .value_kind:     hidden_global_offset_x
      - .offset:         136
        .size:           8
        .value_kind:     hidden_global_offset_y
      - .offset:         144
        .size:           8
        .value_kind:     hidden_global_offset_z
      - .offset:         152
        .size:           2
        .value_kind:     hidden_grid_dims
    .group_segment_fixed_size: 784
    .kernarg_segment_align: 8
    .kernarg_segment_size: 344
    .language:       OpenCL C
    .language_version:
      - 2
      - 0
    .max_flat_workgroup_size: 256
    .name:           _Z4k_U3ILb1EtEvPKtPtPKdPKfS6_PK15HIP_vector_typeIjLj4EES6_PT0_SC_S6_Pd
    .private_segment_fixed_size: 0
    .sgpr_count:     20
    .sgpr_spill_count: 0
    .symbol:         _Z4k_U3ILb1EtEvPKtPtPKdPKfS6_PK15HIP_vector_typeIjLj4EES6_PT0_SC_S6_Pd.kd
    .uniform_work_group_size: 1
    .uses_dynamic_stack: false
    .vgpr_count:     79
    .vgpr_spill_count: 0
    .wavefront_size: 64
